# v34_barmove
# baseline (speedup 1.0000x reference)
.LBB3_39:
	s_andn2_b64 vcc, exec, s[4:5]
	s_cbranch_vccnz .LBB3_197
	v_and_b32_e32 v2, 63, v0
	v_lshrrev_b32_e32 v3, 6, v0
	s_lshl_b32 s34, s2, 2
	s_setprio 3
	v_cmp_ne_u32_e32 vcc, 4, v3
	s_and_saveexec_b64 s[4:5], vcc
	s_xor_b64 s[36:37], exec, s[4:5]
	s_cbranch_execz .LBB3_176
	v_lshrrev_b32_e32 v1, 4, v2
	v_bfe_u32 v65, v0, 2, 2
	v_and_b32_e32 v64, 3, v0
	v_cmp_lt_u32_e32 vcc, 63, v0
	s_waitcnt lgkmcnt(0)
	s_and_saveexec_b64 s[4:5], vcc
	s_xor_b64 s[38:39], exec, s[4:5]
	s_cbranch_execz .LBB3_166
	s_load_dwordx8 s[16:23], s[0:1], 0x100
	s_load_dwordx8 s[24:31], s[0:1], 0xe0
	s_load_dwordx8 s[8:15], s[0:1], 0xc0
	v_and_b32_e32 v105, 15, v0
	v_cmp_lt_i32_e32 vcc, 1, v3
	s_mov_b64 s[40:41], 0
	s_mov_b64 s[6:7], 0
	s_and_saveexec_b64 s[4:5], vcc
	s_xor_b64 s[42:43], exec, s[4:5]
	s_cbranch_execnz .LBB3_46
	s_andn2_saveexec_b64 s[4:5], s[42:43]
	s_cbranch_execnz .LBB3_57

.LBB3_46:
	v_cmp_eq_u32_e32 vcc, 2, v3
	s_mov_b64 s[4:5], -1
	s_and_saveexec_b64 s[44:45], vcc
	s_cbranch_execz .LBB3_56
	v_lshrrev_b32_e32 v2, 2, v2
	v_and_b32_e32 v22, 12, v2
	v_mul_u32_u24_e32 v4, 48, v105
	v_or_b32_e32 v3, v22, v4
	v_lshlrev_b32_e32 v5, 2, v3
	v_or_b32_e32 v24, 3, v2
	v_or_b32_e32 v69, 19, v2
	v_or_b32_e32 v2, 35, v2
	v_or_b32_e32 v3, v24, v4
	v_add_lshl_u32 v26, v69, v4, 2
	v_add_lshl_u32 v4, v2, v4, 2
	v_add_u32_e32 v27, 0xc00, v5
	s_waitcnt lgkmcnt(0)
	global_load_dwordx3 v[6:8], v5, s[12:13]
	global_load_dwordx3 v[10:12], v5, s[14:15]
	v_lshlrev_b32_e32 v25, 2, v3
	global_load_dwordx3 v[14:16], v5, s[12:13] offset:64
	global_load_dwordx3 v[18:20], v5, s[14:15] offset:64
	global_load_dword v3, v25, s[12:13]
	global_load_dword v9, v25, s[14:15]
	global_load_dwordx3 v[32:34], v5, s[12:13] offset:128
	global_load_dwordx3 v[36:38], v5, s[14:15] offset:128
	global_load_dword v13, v26, s[12:13]
	global_load_dword v17, v26, s[14:15]
	global_load_dword v21, v4, s[12:13]
	global_load_dword v23, v4, s[14:15]
	global_load_dwordx3 v[40:42], v27, s[12:13] offset:64
	global_load_dwordx3 v[44:46], v27, s[14:15] offset:64
	global_load_dword v35, v26, s[12:13] offset:3072
	global_load_dword v39, v26, s[14:15] offset:3072
	global_load_dwordx3 v[48:50], v27, s[12:13] offset:128
	global_load_dwordx3 v[52:54], v27, s[14:15] offset:128
	v_mov_b32_e32 v26, 0x600
	v_mad_u32_u24 v73, v105, 48, v26
	global_load_dword v43, v4, s[12:13] offset:3072
	global_load_dword v47, v4, s[14:15] offset:3072
	global_load_dwordx2 v[74:75], v5, s[12:13] offset:3072
	global_load_dwordx2 v[76:77], v5, s[14:15] offset:3072
	global_load_dword v79, v25, s[12:13] offset:3072
	global_load_dword v81, v25, s[14:15] offset:3072
	global_load_dword v78, v27, s[12:13] offset:8
	global_load_dword v80, v27, s[14:15] offset:8
	v_or_b32_e32 v4, v22, v73
	v_lshlrev_b32_e32 v4, 2, v4
	v_add_lshl_u32 v2, v2, v73, 2
	global_load_dwordx3 v[56:58], v4, s[12:13] offset:128
	global_load_dwordx3 v[60:62], v4, s[14:15] offset:128
	global_load_dword v51, v2, s[12:13]
	global_load_dword v55, v2, s[14:15]
	global_load_dwordx3 v[66:68], v4, s[12:13]
	global_load_dwordx3 v[70:72], v4, s[14:15]
	v_or_b32_e32 v2, v24, v73
	v_lshlrev_b32_e32 v2, 2, v2
	global_load_dword v59, v2, s[12:13]
	global_load_dword v63, v2, s[14:15]
	global_load_dwordx3 v[28:30], v4, s[12:13] offset:64
	global_load_dwordx3 v[24:26], v4, s[14:15] offset:64
	v_lshl_or_b32 v31, v64, 4, v22
	v_cmp_eq_u32_e64 s[4:5], 3, v64
	s_mov_b32 s6, 0x4038aa3b
	s_mov_b32 s3, 0x3fb8aa3b
	v_cndmask_b32_e64 v2, v31, 0, s[4:5]
	v_lshlrev_b32_e32 v2, 2, v2
	global_load_dword v27, v2, s[24:25]
	s_mov_b32 s33, 0x3f2aaaab
	v_mov_b32_e32 v4, 0
	v_mov_b32_e32 v5, v4
	s_waitcnt vmcnt(36)
	v_mov_b32_e32 v2, v8
	s_waitcnt vmcnt(35)
	v_pk_mul_f32 v[6:7], v[6:7], v[10:11]
	v_mov_b32_e32 v8, v12
	s_waitcnt vmcnt(33)
	v_pk_mul_f32 v[10:11], v[14:15], v[18:19]
	v_mov_b32_e32 v12, v16
	v_mov_b32_e32 v16, v20
	s_waitcnt vmcnt(29)
	v_pk_mul_f32 v[14:15], v[32:33], v[36:37]
	v_mov_b32_e32 v20, v34
	v_mov_b32_e32 v22, v38
	v_pk_mul_f32 v[2:3], v[2:3], v[8:9]
	v_pk_mul_f32 v[8:9], v[10:11], s[6:7] op_sel_hi:[1,0]
	s_waitcnt vmcnt(27)
	v_pk_mul_f32 v[10:11], v[12:13], v[16:17]
	v_pk_mul_f32 v[12:13], v[14:15], s[6:7] op_sel_hi:[1,0]
	s_waitcnt vmcnt(25)
	v_pk_mul_f32 v[14:15], v[20:21], v[22:23]
	v_pk_mul_f32 v[16:17], v[2:3], s[6:7] op_sel_hi:[1,0]
	v_pk_mul_f32 v[10:11], v[10:11], s[6:7] op_sel_hi:[1,0]
	v_cvt_pk_f16_f32 v2, v12, v13
	v_pk_mul_f32 v[12:13], v[14:15], s[6:7] op_sel_hi:[1,0]
	s_waitcnt vmcnt(24)
	v_mov_b32_e32 v34, v42
	s_waitcnt vmcnt(23)
	v_mov_b32_e32 v38, v46
	s_waitcnt vmcnt(1)
	v_pk_mul_f32 v[24:25], v[28:29], v[24:25]
	v_or_b32_e32 v28, 1, v31
	v_cvt_pk_f16_f32 v8, v8, v9
	v_cvt_pk_f16_f32 v9, v10, v11
	v_cvt_pk_f16_f32 v3, v12, v13
	v_pk_mul_f32 v[10:11], v[40:41], v[44:45]
	v_pk_mul_f32 v[12:13], v[34:35], v[38:39]
	v_cndmask_b32_e64 v28, v28, 0, s[4:5]
	v_or_b32_e32 v29, 2, v31
	v_or_b32_e32 v31, 3, v31
	v_pk_mul_f32 v[10:11], v[10:11], s[6:7] op_sel_hi:[1,0]
	v_pk_mul_f32 v[12:13], v[12:13], s[6:7] op_sel_hi:[1,0]
	v_mov_b32_e32 v42, v50
	v_mov_b32_e32 v46, v54
	v_mov_b32_e32 v50, v58
	v_mov_b32_e32 v54, v62
	v_lshlrev_b32_e32 v28, 2, v28
	v_cndmask_b32_e64 v29, v29, 0, s[4:5]
	v_cndmask_b32_e64 v31, v31, 0, s[4:5]
	v_cvt_pk_f16_f32 v10, v10, v11
	v_cvt_pk_f16_f32 v11, v12, v13
	v_pk_mul_f32 v[12:13], v[48:49], v[52:53]
	v_pk_mul_f32 v[20:21], v[50:51], v[54:55]
	v_lshlrev_b32_e32 v29, 2, v29
	v_lshlrev_b32_e32 v31, 2, v31
	global_load_dword v50, v28, s[24:25]
	global_load_dword v52, v29, s[24:25]
	global_load_dword v54, v31, s[24:25]
	s_waitcnt vmcnt(3)
	v_mul_f32_e32 v28, 0x3fb8aa3b, v27
	v_fma_f32 v29, v27, s3, -v28
	v_rndne_f32_e32 v31, v28
	v_pk_mul_f32 v[14:15], v[42:43], v[46:47]
	v_fmac_f32_e32 v29, 0x32a5705f, v27
	v_sub_f32_e32 v28, v28, v31
	v_pk_mul_f32 v[12:13], v[12:13], s[6:7] op_sel_hi:[1,0]
	v_pk_mul_f32 v[14:15], v[14:15], s[6:7] op_sel_hi:[1,0]
	v_add_f32_e32 v28, v28, v29
	v_cvt_pk_f16_f32 v12, v12, v13
	v_cvt_pk_f16_f32 v13, v14, v15
	v_pk_mul_f32 v[14:15], v[74:75], v[76:77]
	v_exp_f32_e32 v28, v28
	v_cvt_i32_f32_e32 v29, v31
	v_pk_mul_f32 v[6:7], v[6:7], s[6:7] op_sel_hi:[1,0]
	v_pk_mul_f32 v[14:15], v[14:15], s[6:7] op_sel_hi:[1,0]
	v_mov_b32_e32 v58, v68
	v_mov_b32_e32 v62, v72
	v_cvt_pk_f16_f32 v6, v6, v7
	v_cvt_pk_f16_f32 v7, v16, v17
	v_cvt_pk_f16_f32 v16, v14, v15
	v_pk_mul_f32 v[14:15], v[78:79], v[80:81]
	v_pk_mul_f32 v[18:19], v[56:57], v[60:61]
	v_pk_mul_f32 v[22:23], v[66:67], v[70:71]
	v_pk_mul_f32 v[32:33], v[58:59], v[62:63]
	v_pk_mul_f32 v[24:25], v[24:25], s[6:7] op_sel_hi:[1,0]
	v_pk_mul_f32 v[14:15], v[14:15], s[6:7] op_sel_hi:[1,0]
	v_pk_mul_f32 v[18:19], v[18:19], s[6:7] op_sel_hi:[1,0]
	v_pk_mul_f32 v[20:21], v[20:21], s[6:7] op_sel_hi:[1,0]
	v_pk_mul_f32 v[22:23], v[22:23], s[6:7] op_sel_hi:[1,0]
	v_pk_mul_f32 v[32:33], v[32:33], s[6:7] op_sel_hi:[1,0]
	v_cvt_pk_f16_f32 v24, v24, v25
	v_add_lshl_u32 v25, v69, v73, 2
	s_mov_b32 s7, 0xc2ce8ed0
	v_cvt_pk_f16_f32 v22, v22, v23
	v_cvt_pk_f16_f32 v23, v32, v33
	global_load_dword v33, v25, s[12:13]
	global_load_dword v35, v25, s[14:15]
	v_ldexp_f32 v25, v28, v29
	v_cmp_ngt_f32_e32 vcc, s7, v27
	s_mov_b32 s12, 0x42b17218
	v_mov_b32_e32 v32, v30
	v_cndmask_b32_e32 v25, 0, v25, vcc
	v_mov_b32_e32 v30, 0x7f800000
	v_cmp_nlt_f32_e32 vcc, s12, v27
	v_mov_b32_e32 v55, 0x3ecc95a3
	s_mov_b32 s25, 0x3f317218
	v_cndmask_b32_e32 v25, v30, v25, vcc
	v_add_f32_e32 v27, 1.0, v25
	v_add_f32_e32 v28, -1.0, v27
	v_sub_f32_e32 v29, v28, v27
	v_add_f32_e32 v29, 1.0, v29
	v_sub_f32_e32 v28, v25, v28
	v_add_f32_e32 v31, v28, v29
	v_frexp_mant_f32_e32 v34, v27
	v_cvt_f64_f32_e32 v[28:29], v27
	v_frexp_exp_i32_f64_e32 v28, v[28:29]
	v_cmp_gt_f32_e32 vcc, s33, v34
	s_mov_b32 s13, 0x7f800000
	s_mov_b32 s15, 0x33800000
	v_subbrev_co_u32_e32 v34, vcc, 0, v28, vcc
	v_sub_u32_e32 v28, 0, v34
	v_ldexp_f32 v27, v27, v28
	v_ldexp_f32 v28, v31, v28
	v_add_f32_e32 v31, -1.0, v27
	v_add_f32_e32 v29, 1.0, v31
	v_sub_f32_e32 v29, v27, v29
	v_add_f32_e32 v36, v28, v29
	v_add_f32_e32 v29, 1.0, v27
	v_add_f32_e32 v37, -1.0, v29
	v_sub_f32_e32 v27, v27, v37
	v_add_f32_e32 v27, v28, v27
	v_add_f32_e32 v42, v29, v27
	v_rcp_f32_e32 v43, v42
	v_sub_f32_e32 v28, v29, v42
	v_add_f32_e32 v29, v31, v36
	v_add_f32_e32 v27, v27, v28
	v_sub_f32_e32 v28, v31, v29
	v_mul_f32_e32 v44, v29, v43
	v_add_f32_e32 v31, v36, v28
	v_mul_f32_e32 v36, v42, v44
	v_fma_f32 v38, v44, v42, -v36
	v_fmac_f32_e32 v38, v44, v27
	v_add_f32_e32 v28, v36, v38
	v_sub_f32_e32 v37, v29, v28
	v_pk_add_f32 v[40:41], v[28:29], v[36:37] neg_lo:[0,1] neg_hi:[0,1]
	v_mov_b32_e32 v39, v28
	v_pk_add_f32 v[28:29], v[40:41], v[38:39] neg_lo:[0,1] neg_hi:[0,1]
	v_cmp_neq_f32_e32 vcc, s13, v25
	v_add_f32_e32 v29, v31, v29
	v_add_f32_e32 v28, v28, v29
	v_add_f32_e32 v29, v37, v28
	v_mul_f32_e32 v31, v43, v29
	v_mul_f32_e32 v36, v42, v31
	v_fma_f32 v38, v31, v42, -v36
	v_fmac_f32_e32 v38, v31, v27
	v_sub_f32_e32 v27, v37, v29
	v_add_f32_e32 v27, v28, v27
	v_add_f32_e32 v28, v36, v38
	v_sub_f32_e32 v37, v29, v28
	v_pk_add_f32 v[40:41], v[28:29], v[36:37] neg_lo:[0,1] neg_hi:[0,1]
	v_mov_b32_e32 v39, v28
	v_pk_add_f32 v[28:29], v[40:41], v[38:39] neg_lo:[0,1] neg_hi:[0,1]
	v_cvt_f32_i32_e32 v36, v34
	v_add_f32_e32 v27, v27, v29
	v_add_f32_e32 v27, v28, v27
	v_add_f32_e32 v28, v44, v31
	v_add_f32_e32 v27, v37, v27
	v_sub_f32_e32 v29, v28, v44
	v_mul_f32_e32 v27, v43, v27
	v_sub_f32_e32 v29, v31, v29
	v_add_f32_e32 v27, v29, v27
	v_add_f32_e32 v31, v28, v27
	v_mul_f32_e32 v37, v31, v31
	v_fmamk_f32 v29, v37, 0x3e9b6dac, v55
	v_sub_f32_e32 v28, v31, v28
	v_fmaak_f32 v29, v37, v29, 0x3f2aaada
	v_sub_f32_e32 v27, v27, v28
	v_mul_f32_e32 v37, v31, v37
	v_mov_b32_e32 v28, 0x3f317218
	v_pk_mul_f32 v[40:41], v[36:37], v[28:29]
	v_ldexp_f32 v39, v31, 1
	v_fma_f32 v38, v36, s25, -v40
	v_fmac_f32_e32 v38, 0xb102e308, v36
	v_pk_add_f32 v[36:37], v[40:41], v[38:39]
	v_ldexp_f32 v27, v27, 1
	v_sub_f32_e32 v29, v37, v39
	v_sub_f32_e32 v29, v41, v29
	v_add_f32_e32 v43, v27, v29
	v_mov_b32_e32 v42, v40
	v_pk_add_f32 v[40:41], v[36:37], v[40:41] neg_lo:[0,1] neg_hi:[0,1]
	v_pk_add_f32 v[44:45], v[36:37], v[42:43]
	v_mov_b32_e32 v39, v36
	v_mov_b32_e32 v41, v45
	v_pk_add_f32 v[46:47], v[38:39], v[40:41] neg_lo:[0,1] neg_hi:[0,1]
	v_pk_add_f32 v[38:39], v[38:39], v[40:41]
	v_mov_b32_e32 v42, v43
	v_pk_add_f32 v[40:41], v[38:39], v[36:37] op_sel:[1,0] op_sel_hi:[0,1] neg_lo:[0,1] neg_hi:[0,1]
	v_pk_add_f32 v[48:49], v[44:45], v[40:41] op_sel_hi:[1,0] neg_lo:[0,1] neg_hi:[0,1]
	v_mov_b32_e32 v44, v45
	v_mov_b32_e32 v45, v39
	v_pk_mov_b32 v[40:41], v[36:37], v[40:41] op_sel:[1,0]
	v_mov_b32_e32 v43, v36
	v_pk_add_f32 v[40:41], v[44:45], v[40:41] neg_lo:[0,1] neg_hi:[0,1]
	v_mov_b32_e32 v48, v46
	v_pk_add_f32 v[36:37], v[42:43], v[40:41] neg_lo:[0,1] neg_hi:[0,1]
	v_mov_b32_e32 v47, v39
	v_pk_add_f32 v[40:41], v[48:49], v[36:37]
	s_mov_b32 s24, 0x3c23d70a
	v_pk_add_f32 v[42:43], v[40:41], v[40:41] op_sel:[0,1] op_sel_hi:[1,0]
	v_mov_b32_e32 v31, 0x41200000
	v_pk_add_f32 v[38:39], v[38:39], v[42:43] op_sel:[1,0] op_sel_hi:[0,1]
	v_mov_b32_e32 v41, v38
	v_pk_add_f32 v[44:45], v[40:41], v[46:47] neg_lo:[0,1] neg_hi:[0,1]
	v_mov_b32_e32 v37, v42
	v_sub_f32_e32 v27, v40, v44
	v_pk_add_f32 v[36:37], v[36:37], v[44:45] neg_lo:[0,1] neg_hi:[0,1]
	v_sub_f32_e32 v27, v46, v27
	v_add_f32_e32 v27, v36, v27
	v_add_f32_e32 v27, v27, v37
	v_add_f32_e32 v27, v38, v27
	v_cndmask_b32_e32 v27, v30, v27, vcc
	v_cmp_lt_f32_e64 vcc, |v25|, s15
	s_mov_b32 s14, 0xbd23d70a
	v_mov_b32_e32 v34, v26
	v_cndmask_b32_e32 v25, v27, v25, vcc
	v_add_f32_e32 v25, 0x358637bd, v25
	v_med3_f32 v25, v25, s24, v31
	v_div_scale_f32 v29, s[46:47], v25, v25, s14
	v_rcp_f32_e32 v36, v29
	s_waitcnt vmcnt(0)
	v_pk_mul_f32 v[26:27], v[32:33], v[34:35]
	v_mov_b32_e32 v49, 0x3f2aaada
	v_pk_mul_f32 v[26:27], v[26:27], s[6:7] op_sel_hi:[1,0]
	v_fma_f32 v32, -v29, v36, 1.0
	v_fmac_f32_e32 v36, v32, v36
	v_div_scale_f32 v32, vcc, s14, v25, s14
	v_mul_f32_e32 v33, v32, v36
	v_fma_f32 v34, -v29, v33, v32
	v_fmac_f32_e32 v33, v34, v36
	v_fma_f32 v29, -v29, v33, v32
	v_div_fmas_f32 v29, v29, v36, v33
	v_mul_f32_e32 v33, 0x3fb8aa3b, v50
	v_fma_f32 v34, v50, s3, -v33
	v_rndne_f32_e32 v35, v33
	v_fmac_f32_e32 v34, 0x32a5705f, v50
	v_sub_f32_e32 v33, v33, v35
	v_div_fixup_f32 v46, v29, v25, s14
	v_add_f32_e32 v33, v33, v34
	v_mul_f32_e32 v25, 0x3fb8aa3b, v46
	v_exp_f32_e32 v33, v33
	v_cvt_i32_f32_e32 v34, v35
	v_fma_f32 v29, v46, s3, -v25
	v_rndne_f32_e32 v32, v25
	v_fmac_f32_e32 v29, 0x32a5705f, v46
	v_sub_f32_e32 v25, v25, v32
	v_add_f32_e32 v25, v25, v29
	v_exp_f32_e32 v47, v25
	v_ldexp_f32 v25, v33, v34
	v_cmp_ngt_f32_e32 vcc, s7, v50
	v_cvt_i32_f32_e32 v48, v32
	v_cvt_pk_f16_f32 v17, v14, v15
	v_cndmask_b32_e32 v25, 0, v25, vcc
	v_cmp_nlt_f32_e32 vcc, s12, v50
	v_mov_b32_e32 v14, v4
	v_mov_b32_e32 v15, v4
	v_cndmask_b32_e32 v25, v30, v25, vcc
	v_add_f32_e32 v29, 1.0, v25
	v_add_f32_e32 v32, -1.0, v29
	v_sub_f32_e32 v33, v32, v29
	v_add_f32_e32 v33, 1.0, v33
	v_sub_f32_e32 v32, v25, v32
	v_add_f32_e32 v34, v32, v33
	v_frexp_mant_f32_e32 v35, v29
	v_cvt_f64_f32_e32 v[32:33], v29
	v_frexp_exp_i32_f64_e32 v32, v[32:33]
	v_cmp_gt_f32_e32 vcc, s33, v35
	v_cvt_pk_f16_f32 v18, v18, v19
	v_cvt_pk_f16_f32 v19, v20, v21
	v_subbrev_co_u32_e32 v40, vcc, 0, v32, vcc
	v_sub_u32_e32 v32, 0, v40
	v_ldexp_f32 v29, v29, v32
	v_ldexp_f32 v32, v34, v32
	v_add_f32_e32 v34, -1.0, v29
	v_add_f32_e32 v33, 1.0, v34
	v_sub_f32_e32 v33, v29, v33
	v_add_f32_e32 v35, v32, v33
	v_add_f32_e32 v33, 1.0, v29
	v_add_f32_e32 v36, -1.0, v33
	v_sub_f32_e32 v29, v29, v36
	v_add_f32_e32 v29, v32, v29
	v_add_f32_e32 v41, v33, v29
	v_rcp_f32_e32 v42, v41
	v_sub_f32_e32 v32, v33, v41
	v_add_f32_e32 v33, v34, v35
	v_add_f32_e32 v29, v29, v32
	v_mul_f32_e32 v44, v33, v42
	v_sub_f32_e32 v32, v34, v33
	v_mul_f32_e32 v34, v41, v44
	v_fma_f32 v36, v44, v41, -v34
	v_fmac_f32_e32 v36, v44, v29
	v_add_f32_e32 v43, v35, v32
	v_add_f32_e32 v32, v34, v36
	v_sub_f32_e32 v35, v33, v32
	v_pk_add_f32 v[38:39], v[32:33], v[34:35] neg_lo:[0,1] neg_hi:[0,1]
	v_mov_b32_e32 v37, v32
	v_pk_add_f32 v[32:33], v[38:39], v[36:37] neg_lo:[0,1] neg_hi:[0,1]
	v_cmp_neq_f32_e32 vcc, s13, v25
	v_add_f32_e32 v33, v43, v33
	v_add_f32_e32 v32, v32, v33
	v_add_f32_e32 v33, v35, v32
	v_mul_f32_e32 v43, v42, v33
	v_mul_f32_e32 v34, v41, v43
	v_fma_f32 v36, v43, v41, -v34
	v_fmac_f32_e32 v36, v43, v29
	v_sub_f32_e32 v29, v35, v33
	v_add_f32_e32 v29, v32, v29
	v_add_f32_e32 v32, v34, v36
	v_sub_f32_e32 v35, v33, v32
	v_pk_add_f32 v[38:39], v[32:33], v[34:35] neg_lo:[0,1] neg_hi:[0,1]
	v_mov_b32_e32 v37, v32
	v_pk_add_f32 v[32:33], v[38:39], v[36:37] neg_lo:[0,1] neg_hi:[0,1]
	v_mov_b32_e32 v20, v4
	v_add_f32_e32 v29, v29, v33
	v_add_f32_e32 v29, v32, v29
	v_add_f32_e32 v33, v44, v43
	v_add_f32_e32 v29, v35, v29
	v_sub_f32_e32 v32, v33, v44
	v_mul_f32_e32 v29, v42, v29
	v_sub_f32_e32 v32, v43, v32
	v_add_f32_e32 v34, v32, v29
	v_add_f32_e32 v36, v33, v34
	v_cvt_f32_i32_e32 v32, v40
	v_mul_f32_e32 v37, v36, v36
	v_sub_f32_e32 v33, v36, v33
	v_fmamk_f32 v29, v37, 0x3e9b6dac, v55
	v_sub_f32_e32 v33, v34, v33
	v_fmaak_f32 v29, v37, v29, 0x3f2aaada
	v_ldexp_f32 v38, v33, 1
	v_mul_f32_e32 v33, v36, v37
	v_ldexp_f32 v35, v36, 1
	v_pk_mul_f32 v[36:37], v[32:33], v[28:29]
	v_mov_b32_e32 v21, v4
	v_fma_f32 v34, v32, s25, -v36
	v_fmac_f32_e32 v34, 0xb102e308, v32
	v_pk_add_f32 v[32:33], v[36:37], v[34:35]
	s_nop 0
	v_sub_f32_e32 v29, v33, v35
	v_sub_f32_e32 v29, v37, v29
	v_add_f32_e32 v39, v38, v29
	v_mov_b32_e32 v38, v36
	v_pk_add_f32 v[36:37], v[32:33], v[36:37] neg_lo:[0,1] neg_hi:[0,1]
	v_pk_add_f32 v[40:41], v[32:33], v[38:39]
	v_mov_b32_e32 v35, v32
	v_mov_b32_e32 v37, v41
	v_pk_add_f32 v[42:43], v[34:35], v[36:37] neg_lo:[0,1] neg_hi:[0,1]
	v_pk_add_f32 v[34:35], v[34:35], v[36:37]
	v_mov_b32_e32 v38, v39
	v_pk_add_f32 v[36:37], v[34:35], v[32:33] op_sel:[1,0] op_sel_hi:[0,1] neg_lo:[0,1] neg_hi:[0,1]
	v_pk_add_f32 v[44:45], v[40:41], v[36:37] op_sel_hi:[1,0] neg_lo:[0,1] neg_hi:[0,1]
	v_mov_b32_e32 v40, v41
	v_mov_b32_e32 v41, v35
	v_pk_mov_b32 v[36:37], v[32:33], v[36:37] op_sel:[1,0]
	v_mov_b32_e32 v39, v32
	v_pk_add_f32 v[36:37], v[40:41], v[36:37] neg_lo:[0,1] neg_hi:[0,1]
	v_mov_b32_e32 v44, v42
	v_pk_add_f32 v[32:33], v[38:39], v[36:37] neg_lo:[0,1] neg_hi:[0,1]
	v_mov_b32_e32 v43, v35
	v_pk_add_f32 v[36:37], v[44:45], v[32:33]
	s_nop 0
	v_pk_add_f32 v[38:39], v[36:37], v[36:37] op_sel:[0,1] op_sel_hi:[1,0]
	s_nop 0
	v_pk_add_f32 v[34:35], v[34:35], v[38:39] op_sel:[1,0] op_sel_hi:[0,1]
	v_mov_b32_e32 v37, v34
	v_pk_add_f32 v[40:41], v[36:37], v[42:43] neg_lo:[0,1] neg_hi:[0,1]
	v_mov_b32_e32 v33, v38
	v_sub_f32_e32 v29, v36, v40
	v_pk_add_f32 v[32:33], v[32:33], v[40:41] neg_lo:[0,1] neg_hi:[0,1]
	v_sub_f32_e32 v29, v42, v29
	v_add_f32_e32 v29, v32, v29
	v_add_f32_e32 v29, v29, v33
	v_add_f32_e32 v29, v34, v29
	v_cndmask_b32_e32 v29, v30, v29, vcc
	v_cmp_lt_f32_e64 vcc, |v25|, s15
	s_nop 1
	v_cndmask_b32_e32 v25, v29, v25, vcc
	v_add_f32_e32 v25, 0x358637bd, v25
	v_med3_f32 v29, v25, s24, v31
	v_div_scale_f32 v32, s[46:47], v29, v29, s14
	v_rcp_f32_e32 v33, v32
	v_cvt_pk_f16_f32 v25, v26, v27
	v_ldexp_f32 v26, v47, v48
	v_fma_f32 v27, -v32, v33, 1.0
	v_fmac_f32_e32 v33, v27, v33
	v_div_scale_f32 v27, vcc, s14, v29, s14
	v_mul_f32_e32 v34, v27, v33
	v_fma_f32 v35, -v32, v34, v27
	v_fmac_f32_e32 v34, v35, v33
	v_fma_f32 v27, -v32, v34, v27
	v_div_fmas_f32 v27, v27, v33, v34
	v_div_fixup_f32 v27, v27, v29, s14
	v_mul_f32_e32 v29, 0x3fb8aa3b, v27
	v_fma_f32 v32, v27, s3, -v29
	v_rndne_f32_e32 v33, v29
	v_fmac_f32_e32 v32, 0x32a5705f, v27
	v_sub_f32_e32 v29, v29, v33
	v_add_f32_e32 v29, v29, v32
	v_exp_f32_e32 v29, v29
	v_cvt_i32_f32_e32 v32, v33
	v_cmp_ngt_f32_e32 vcc, s7, v46
	v_ldexp_f32 v29, v29, v32
	s_nop 0
	v_cndmask_b32_e32 v26, 0, v26, vcc
	v_cmp_nlt_f32_e32 vcc, s12, v46
	s_nop 1
	v_cndmask_b32_e32 v26, v30, v26, vcc
	v_cmp_ngt_f32_e32 vcc, s7, v27
	v_cndmask_b32_e64 v50, v26, 0, s[4:5]
	s_nop 0
	v_cndmask_b32_e32 v29, 0, v29, vcc
	v_cmp_nlt_f32_e32 vcc, s12, v27
	s_nop 1
	v_cndmask_b32_e32 v27, v30, v29, vcc
	v_mul_f32_e32 v29, 0x3fb8aa3b, v52
	v_fma_f32 v32, v52, s3, -v29
	v_rndne_f32_e32 v33, v29
	v_fmac_f32_e32 v32, 0x32a5705f, v52
	v_sub_f32_e32 v29, v29, v33
	v_add_f32_e32 v29, v29, v32
	v_exp_f32_e32 v29, v29
	v_cvt_i32_f32_e32 v32, v33
	v_cmp_ngt_f32_e32 vcc, s7, v52
	v_cndmask_b32_e64 v51, v27, 0, s[4:5]
	v_pk_add_f32 v[26:27], v[26:27], 1.0 op_sel_hi:[1,0] neg_lo:[1,0] neg_hi:[1,0]
	v_ldexp_f32 v29, v29, v32
	v_cndmask_b32_e32 v29, 0, v29, vcc
	v_cmp_nlt_f32_e32 vcc, s12, v52
	v_cndmask_b32_e64 v52, v26, 0, s[4:5]
	v_cndmask_b32_e64 v53, v27, 0, s[4:5]
	v_cndmask_b32_e32 v46, v30, v29, vcc
	v_add_f32_e32 v29, 1.0, v46
	v_add_f32_e32 v32, -1.0, v29
	v_sub_f32_e32 v33, v32, v29
	v_add_f32_e32 v33, 1.0, v33
	v_sub_f32_e32 v32, v46, v32
	v_add_f32_e32 v34, v32, v33
	v_frexp_mant_f32_e32 v35, v29
	v_cvt_f64_f32_e32 v[32:33], v29
	v_frexp_exp_i32_f64_e32 v32, v[32:33]
	v_cmp_gt_f32_e32 vcc, s33, v35
	s_nop 1
	v_subbrev_co_u32_e32 v40, vcc, 0, v32, vcc
	v_sub_u32_e32 v32, 0, v40
	v_ldexp_f32 v29, v29, v32
	v_ldexp_f32 v32, v34, v32
	v_add_f32_e32 v34, -1.0, v29
	v_add_f32_e32 v33, 1.0, v34
	v_sub_f32_e32 v33, v29, v33
	v_add_f32_e32 v35, v32, v33
	v_add_f32_e32 v33, 1.0, v29
	v_add_f32_e32 v36, -1.0, v33
	v_sub_f32_e32 v29, v29, v36
	v_add_f32_e32 v29, v32, v29
	v_add_f32_e32 v41, v33, v29
	v_rcp_f32_e32 v42, v41
	v_sub_f32_e32 v32, v33, v41
	v_add_f32_e32 v33, v34, v35
	v_add_f32_e32 v29, v29, v32
	v_mul_f32_e32 v44, v33, v42
	v_sub_f32_e32 v32, v34, v33
	v_mul_f32_e32 v34, v41, v44
	v_fma_f32 v36, v44, v41, -v34
	v_fmac_f32_e32 v36, v44, v29
	v_add_f32_e32 v43, v35, v32
	v_add_f32_e32 v32, v34, v36
	v_sub_f32_e32 v35, v33, v32
	v_pk_add_f32 v[38:39], v[32:33], v[34:35] neg_lo:[0,1] neg_hi:[0,1]
	v_mov_b32_e32 v37, v32
	v_pk_add_f32 v[32:33], v[38:39], v[36:37] neg_lo:[0,1] neg_hi:[0,1]
	v_cmp_neq_f32_e32 vcc, s13, v46
	v_add_f32_e32 v33, v43, v33
	v_add_f32_e32 v32, v32, v33
	v_add_f32_e32 v33, v35, v32
	v_mul_f32_e32 v43, v42, v33
	v_mul_f32_e32 v34, v41, v43
	v_fma_f32 v36, v43, v41, -v34
	v_fmac_f32_e32 v36, v43, v29
	v_sub_f32_e32 v29, v35, v33
	v_add_f32_e32 v29, v32, v29
	v_add_f32_e32 v32, v34, v36
	v_sub_f32_e32 v35, v33, v32
	v_pk_add_f32 v[38:39], v[32:33], v[34:35] neg_lo:[0,1] neg_hi:[0,1]
	v_mov_b32_e32 v37, v32
	v_pk_add_f32 v[32:33], v[38:39], v[36:37] neg_lo:[0,1] neg_hi:[0,1]
	s_nop 0
	v_add_f32_e32 v29, v29, v33
	v_add_f32_e32 v29, v32, v29
	v_add_f32_e32 v33, v44, v43
	v_add_f32_e32 v29, v35, v29
	v_sub_f32_e32 v32, v33, v44
	v_mul_f32_e32 v29, v42, v29
	v_sub_f32_e32 v32, v43, v32
	v_add_f32_e32 v34, v32, v29
	v_add_f32_e32 v36, v33, v34
	v_cvt_f32_i32_e32 v32, v40
	v_mul_f32_e32 v37, v36, v36
	v_sub_f32_e32 v33, v36, v33
	v_fmamk_f32 v29, v37, 0x3e9b6dac, v55
	v_sub_f32_e32 v33, v34, v33
	v_fmaak_f32 v29, v37, v29, 0x3f2aaada
	v_ldexp_f32 v38, v33, 1
	v_mul_f32_e32 v33, v36, v37
	v_ldexp_f32 v35, v36, 1
	v_pk_mul_f32 v[36:37], v[32:33], v[28:29]
	s_nop 0
	v_fma_f32 v34, v32, s25, -v36
	v_fmac_f32_e32 v34, 0xb102e308, v32
	v_pk_add_f32 v[32:33], v[36:37], v[34:35]
	s_nop 0
	v_sub_f32_e32 v29, v33, v35
	v_sub_f32_e32 v29, v37, v29
	v_add_f32_e32 v39, v38, v29
	v_mov_b32_e32 v38, v36
	v_pk_add_f32 v[36:37], v[32:33], v[36:37] neg_lo:[0,1] neg_hi:[0,1]
	v_pk_add_f32 v[40:41], v[32:33], v[38:39]
	v_mov_b32_e32 v35, v32
	v_mov_b32_e32 v37, v41
	v_pk_add_f32 v[42:43], v[34:35], v[36:37] neg_lo:[0,1] neg_hi:[0,1]
	v_pk_add_f32 v[34:35], v[34:35], v[36:37]
	v_mov_b32_e32 v38, v39
	v_pk_add_f32 v[36:37], v[34:35], v[32:33] op_sel:[1,0] op_sel_hi:[0,1] neg_lo:[0,1] neg_hi:[0,1]
	v_pk_add_f32 v[44:45], v[40:41], v[36:37] op_sel_hi:[1,0] neg_lo:[0,1] neg_hi:[0,1]
	v_mov_b32_e32 v40, v41
	v_mov_b32_e32 v41, v35
	v_pk_mov_b32 v[36:37], v[32:33], v[36:37] op_sel:[1,0]
	v_mov_b32_e32 v39, v32
	v_pk_add_f32 v[36:37], v[40:41], v[36:37] neg_lo:[0,1] neg_hi:[0,1]
	v_mov_b32_e32 v44, v42
	v_pk_add_f32 v[32:33], v[38:39], v[36:37] neg_lo:[0,1] neg_hi:[0,1]
	v_mov_b32_e32 v43, v35
	v_pk_add_f32 v[36:37], v[44:45], v[32:33]
	s_nop 0
	v_pk_add_f32 v[38:39], v[36:37], v[36:37] op_sel:[0,1] op_sel_hi:[1,0]
	s_nop 0
	v_pk_add_f32 v[34:35], v[34:35], v[38:39] op_sel:[1,0] op_sel_hi:[0,1]
	v_mov_b32_e32 v37, v34
	v_pk_add_f32 v[40:41], v[36:37], v[42:43] neg_lo:[0,1] neg_hi:[0,1]
	v_mov_b32_e32 v33, v38
	v_sub_f32_e32 v29, v36, v40
	v_pk_add_f32 v[32:33], v[32:33], v[40:41] neg_lo:[0,1] neg_hi:[0,1]
	v_sub_f32_e32 v29, v42, v29
	v_add_f32_e32 v29, v32, v29
	v_add_f32_e32 v29, v29, v33
	v_add_f32_e32 v29, v34, v29
	v_cndmask_b32_e32 v29, v30, v29, vcc
	v_cmp_lt_f32_e64 vcc, |v46|, s15
	v_pk_mul_f32 v[32:33], v[26:27], -2.0 op_sel_hi:[1,0]
	s_nop 0
	v_cndmask_b32_e32 v29, v29, v46, vcc
	v_add_f32_e32 v29, 0x358637bd, v29
	v_med3_f32 v29, v29, s24, v31
	v_div_scale_f32 v34, s[46:47], v29, v29, s14
	v_rcp_f32_e32 v35, v34
	s_nop 0
	v_fma_f32 v26, -v34, v35, 1.0
	v_fmac_f32_e32 v35, v26, v35
	v_div_scale_f32 v26, vcc, s14, v29, s14
	v_mul_f32_e32 v27, v26, v35
	v_fma_f32 v36, -v34, v27, v26
	v_fmac_f32_e32 v27, v36, v35
	v_fma_f32 v26, -v34, v27, v26
	v_mul_f32_e32 v34, 0x3fb8aa3b, v54
	v_div_fmas_f32 v26, v26, v35, v27
	v_fma_f32 v35, v54, s3, -v34
	v_rndne_f32_e32 v36, v34
	v_fmac_f32_e32 v35, 0x32a5705f, v54
	v_sub_f32_e32 v34, v34, v36
	v_div_fixup_f32 v44, v26, v29, s14
	v_add_f32_e32 v34, v34, v35
	v_mul_f32_e32 v26, 0x3fb8aa3b, v44
	v_exp_f32_e32 v34, v34
	v_cvt_i32_f32_e32 v35, v36
	v_fma_f32 v27, v44, s3, -v26
	v_rndne_f32_e32 v29, v26
	v_fmac_f32_e32 v27, 0x32a5705f, v44
	v_sub_f32_e32 v26, v26, v29
	v_add_f32_e32 v26, v26, v27
	v_exp_f32_e32 v45, v26
	v_ldexp_f32 v26, v34, v35
	v_cmp_ngt_f32_e32 vcc, s7, v54
	v_cvt_i32_f32_e32 v46, v29
	s_nop 0
	v_cndmask_b32_e32 v26, 0, v26, vcc
	v_cmp_nlt_f32_e32 vcc, s12, v54
	v_cndmask_b32_e64 v54, v32, 0, s[4:5]
	s_nop 0
	v_cndmask_b32_e32 v47, v30, v26, vcc
	v_add_f32_e32 v29, 1.0, v47
	v_add_f32_e32 v26, -1.0, v29
	v_sub_f32_e32 v27, v26, v29
	v_add_f32_e32 v27, 1.0, v27
	v_sub_f32_e32 v26, v47, v26
	v_add_f32_e32 v34, v26, v27
	v_frexp_mant_f32_e32 v35, v29
	v_cvt_f64_f32_e32 v[26:27], v29
	v_frexp_exp_i32_f64_e32 v26, v[26:27]
	v_cmp_gt_f32_e32 vcc, s33, v35
	s_nop 1
	v_subbrev_co_u32_e32 v40, vcc, 0, v26, vcc
	v_sub_u32_e32 v26, 0, v40
	v_ldexp_f32 v27, v29, v26
	v_add_f32_e32 v29, -1.0, v27
	v_add_f32_e32 v35, 1.0, v27
	v_ldexp_f32 v26, v34, v26
	v_add_f32_e32 v34, 1.0, v29
	v_add_f32_e32 v36, -1.0, v35
	v_sub_f32_e32 v34, v27, v34
	v_sub_f32_e32 v27, v27, v36
	v_add_f32_e32 v34, v26, v34
	v_add_f32_e32 v26, v26, v27
	v_add_f32_e32 v41, v35, v26
	v_rcp_f32_e32 v43, v41
	v_sub_f32_e32 v27, v35, v41
	v_add_f32_e32 v42, v26, v27
	v_add_f32_e32 v27, v29, v34
	v_sub_f32_e32 v26, v29, v27
	v_mul_f32_e32 v48, v27, v43
	v_add_f32_e32 v29, v34, v26
	v_mul_f32_e32 v34, v41, v48
	v_fma_f32 v36, v48, v41, -v34
	v_fmac_f32_e32 v36, v48, v42
	v_add_f32_e32 v26, v34, v36
	v_sub_f32_e32 v35, v27, v26
	v_pk_add_f32 v[38:39], v[26:27], v[34:35] neg_lo:[0,1] neg_hi:[0,1]
	v_mov_b32_e32 v37, v26
	v_pk_add_f32 v[26:27], v[38:39], v[36:37] neg_lo:[0,1] neg_hi:[0,1]
	v_cmp_neq_f32_e32 vcc, s13, v47
	v_add_f32_e32 v27, v29, v27
	v_add_f32_e32 v26, v26, v27
	v_add_f32_e32 v27, v35, v26
	v_mul_f32_e32 v29, v43, v27
	v_mul_f32_e32 v34, v41, v29
	v_fma_f32 v36, v29, v41, -v34
	v_fmac_f32_e32 v36, v29, v42
	v_sub_f32_e32 v35, v35, v27
	v_add_f32_e32 v41, v26, v35
	v_add_f32_e32 v26, v34, v36
	v_sub_f32_e32 v35, v27, v26
	v_pk_add_f32 v[38:39], v[26:27], v[34:35] neg_lo:[0,1] neg_hi:[0,1]
	v_mov_b32_e32 v37, v26
	v_pk_add_f32 v[26:27], v[38:39], v[36:37] neg_lo:[0,1] neg_hi:[0,1]
	s_nop 0
	v_add_f32_e32 v27, v41, v27
	v_add_f32_e32 v26, v26, v27
	v_add_f32_e32 v27, v48, v29
	v_add_f32_e32 v26, v35, v26
	v_sub_f32_e32 v34, v27, v48
	v_mul_f32_e32 v26, v43, v26
	v_sub_f32_e32 v29, v29, v34
	v_add_f32_e32 v29, v29, v26
	v_add_f32_e32 v34, v27, v29
	v_mul_f32_e32 v36, v34, v34
	v_cvt_f32_i32_e32 v26, v40
	v_fmac_f32_e32 v55, 0x3e9b6dac, v36
	v_sub_f32_e32 v27, v34, v27
	v_fmac_f32_e32 v49, v36, v55
	v_sub_f32_e32 v27, v29, v27
	v_ldexp_f32 v37, v27, 1
	v_mul_f32_e32 v27, v34, v36
	v_mov_b32_e32 v29, v49
	v_pk_mul_f32 v[28:29], v[26:27], v[28:29]
	v_ldexp_f32 v35, v34, 1
	v_fma_f32 v34, v26, s25, -v28
	v_fmac_f32_e32 v34, 0xb102e308, v26
	v_pk_add_f32 v[26:27], v[28:29], v[34:35]
	v_mov_b32_e32 v36, v28
	v_sub_f32_e32 v35, v27, v35
	v_sub_f32_e32 v35, v29, v35
	v_add_f32_e32 v37, v37, v35
	v_pk_add_f32 v[28:29], v[26:27], v[28:29] neg_lo:[0,1] neg_hi:[0,1]
	v_pk_add_f32 v[38:39], v[26:27], v[36:37]
	v_mov_b32_e32 v35, v26
	v_mov_b32_e32 v29, v39
	v_pk_add_f32 v[40:41], v[34:35], v[28:29] neg_lo:[0,1] neg_hi:[0,1]
	v_pk_add_f32 v[28:29], v[34:35], v[28:29]
	v_mov_b32_e32 v36, v37
	v_pk_add_f32 v[34:35], v[28:29], v[26:27] op_sel:[1,0] op_sel_hi:[0,1] neg_lo:[0,1] neg_hi:[0,1]
	v_pk_add_f32 v[42:43], v[38:39], v[34:35] op_sel_hi:[1,0] neg_lo:[0,1] neg_hi:[0,1]
	v_mov_b32_e32 v38, v39
	v_mov_b32_e32 v39, v29
	v_pk_mov_b32 v[34:35], v[26:27], v[34:35] op_sel:[1,0]
	v_mov_b32_e32 v37, v26
	v_pk_add_f32 v[34:35], v[38:39], v[34:35] neg_lo:[0,1] neg_hi:[0,1]
	v_mov_b32_e32 v42, v40
	v_pk_add_f32 v[26:27], v[36:37], v[34:35] neg_lo:[0,1] neg_hi:[0,1]
	v_mov_b32_e32 v41, v29
	v_pk_add_f32 v[34:35], v[42:43], v[26:27]
	v_cndmask_b32_e64 v55, v33, 0, s[4:5]
	v_pk_add_f32 v[36:37], v[34:35], v[34:35] op_sel:[0,1] op_sel_hi:[1,0]
	s_nop 0
	v_pk_add_f32 v[28:29], v[28:29], v[36:37] op_sel:[1,0] op_sel_hi:[0,1]
	v_mov_b32_e32 v35, v28
	v_pk_add_f32 v[38:39], v[34:35], v[40:41] neg_lo:[0,1] neg_hi:[0,1]
	v_mov_b32_e32 v27, v36
	v_sub_f32_e32 v29, v34, v38
	v_pk_add_f32 v[26:27], v[26:27], v[38:39] neg_lo:[0,1] neg_hi:[0,1]
	v_sub_f32_e32 v29, v40, v29
	v_add_f32_e32 v26, v26, v29
	v_add_f32_e32 v26, v26, v27
	v_add_f32_e32 v26, v28, v26
	v_cndmask_b32_e32 v26, v30, v26, vcc
	v_cmp_lt_f32_e64 vcc, |v47|, s15
	v_ldexp_f32 v29, v45, v46
	s_nop 0
	v_cndmask_b32_e32 v26, v26, v47, vcc
	v_add_f32_e32 v26, 0x358637bd, v26
	v_med3_f32 v26, v26, s24, v31
	v_div_scale_f32 v27, s[24:25], v26, v26, s14
	v_rcp_f32_e32 v28, v27
	s_nop 0
	v_fma_f32 v31, -v27, v28, 1.0
	v_fmac_f32_e32 v28, v31, v28
	v_div_scale_f32 v31, vcc, s14, v26, s14
	v_mul_f32_e32 v32, v31, v28
	v_fma_f32 v33, -v27, v32, v31
	v_fmac_f32_e32 v32, v33, v28
	v_fma_f32 v27, -v27, v32, v31
	v_div_fmas_f32 v27, v27, v28, v32
	v_div_fixup_f32 v27, v27, v26, s14
	v_mul_f32_e32 v26, 0x3fb8aa3b, v27
	v_fma_f32 v28, v27, s3, -v26
	v_rndne_f32_e32 v31, v26
	v_fmac_f32_e32 v28, 0x32a5705f, v27
	v_sub_f32_e32 v26, v26, v31
	v_add_f32_e32 v26, v26, v28
	v_exp_f32_e32 v28, v26
	v_cvt_i32_f32_e32 v31, v31
	v_cmp_ngt_f32_e32 vcc, s7, v44
	s_movk_i32 s3, 0xc0
	v_mov_b32_e32 v32, v4
	v_cndmask_b32_e32 v26, 0, v29, vcc
	v_cmp_nlt_f32_e32 vcc, s12, v44
	v_ldexp_f32 v28, v28, v31
	v_mov_b32_e32 v31, v4
	v_cndmask_b32_e32 v26, v30, v26, vcc
	v_cmp_ngt_f32_e32 vcc, s7, v27
	v_cndmask_b32_e64 v56, v26, 0, s[4:5]
	v_cmp_eq_u32_e64 s[6:7], 0, v64
	v_cndmask_b32_e32 v28, 0, v28, vcc
	v_cmp_nlt_f32_e32 vcc, s12, v27
	v_mov_b32_e32 v33, v4
	s_nop 0
	v_cndmask_b32_e32 v27, v30, v28, vcc
	v_cndmask_b32_e64 v57, v27, 0, s[4:5]
	v_pk_add_f32 v[26:27], v[26:27], 1.0 op_sel_hi:[1,0] neg_lo:[1,0] neg_hi:[1,0]
	v_mov_b32_e32 v30, v4
	v_pk_mul_f32 v[28:29], v[26:27], -2.0 op_sel_hi:[1,0]
	v_cndmask_b32_e64 v59, v27, 0, s[4:5]
	v_cndmask_b32_e64 v60, v28, 0, s[4:5]
	v_lshlrev_b32_e32 v27, 6, v64
	v_mov_b32_e32 v28, 0x80
	v_cndmask_b32_e64 v27, v27, v28, s[4:5]
	v_mad_u32_u24 v27, v65, s3, v27
	v_cndmask_b32_e64 v58, v26, 0, s[4:5]
	v_mul_u32_u24_e32 v26, 0xc0, v65
	v_and_or_b32 v62, v0, 48, v27
	v_lshlrev_b32_e32 v27, 6, v65
	v_sub_u32_e32 v26, v26, v27
	v_lshl_add_u32 v26, v1, 5, v26
	v_cndmask_b32_e64 v61, v29, 0, s[4:5]
	v_lshl_or_b32 v63, v64, 3, v26
	v_cmp_gt_u32_e64 s[4:5], 2, v64
	s_mov_b32 s3, -2
	v_mov_b32_e32 v166, v6
	v_mov_b32_e32 v167, v7
	v_mov_b32_e32 v168, v8
	v_mov_b32_e32 v169, v9
	v_mov_b32_e32 v170, v2
	v_mov_b32_e32 v171, v3
	v_mov_b32_e32 v172, v4
	v_mov_b32_e32 v173, v5
	v_mov_b32_e32 v6, v166
	v_mov_b32_e32 v7, v168
	v_mov_b32_e32 v8, v170
	v_mov_b32_e32 v9, v172
	v_mov_b32_e32 v2, v167
	v_mov_b32_e32 v3, v169
	v_mov_b32_e32 v4, v171
	v_mov_b32_e32 v5, v173
	v_mov_b32_e32 v166, v10
	v_mov_b32_e32 v167, v11
	v_mov_b32_e32 v168, v12
	v_mov_b32_e32 v169, v13
	v_mov_b32_e32 v170, v14
	v_mov_b32_e32 v171, v15
	v_mov_b32_e32 v172, v16
	v_mov_b32_e32 v173, v17
	v_mov_b32_e32 v10, v166
	v_mov_b32_e32 v11, v168
	v_mov_b32_e32 v12, v170
	v_mov_b32_e32 v13, v172
	v_mov_b32_e32 v14, v167
	v_mov_b32_e32 v15, v169
	v_mov_b32_e32 v16, v171
	v_mov_b32_e32 v17, v173
	v_mov_b32_e32 v166, v18
	v_mov_b32_e32 v167, v19
	v_mov_b32_e32 v168, v20
	v_mov_b32_e32 v169, v21
	v_mov_b32_e32 v170, v22
	v_mov_b32_e32 v171, v23
	v_mov_b32_e32 v172, v24
	v_mov_b32_e32 v173, v25
	v_mov_b32_e32 v18, v166
	v_mov_b32_e32 v19, v168
	v_mov_b32_e32 v20, v170
	v_mov_b32_e32 v21, v172
	v_mov_b32_e32 v22, v167
	v_mov_b32_e32 v23, v169
	v_mov_b32_e32 v24, v171
	v_mov_b32_e32 v25, v173
	v_mov_b32_e32 v124, 0
	v_mov_b32_e32 v125, 0
	v_mov_b32_e32 v126, 0
	v_mov_b32_e32 v127, 0
	v_mov_b32_e32 v128, 0
	v_mov_b32_e32 v129, 0
	v_mov_b32_e32 v130, 0
	v_mov_b32_e32 v131, 0
	v_mov_b32_e32 v148, 0
	v_mov_b32_e32 v149, 0
	v_mov_b32_e32 v150, 0
	v_mov_b32_e32 v151, 0
	v_mov_b32_e32 v168, 0
	v_mov_b32_e32 v169, 0
	v_mov_b32_e32 v170, 0
	v_mov_b32_e32 v171, 0
	v_mov_b32_e32 v152, v52
	v_mov_b32_e32 v153, v53
	v_mov_b32_e32 v154, v58
	v_mov_b32_e32 v155, v59
	s_waitcnt lgkmcnt(0)
	s_barrier
	s_barrier
	s_waitcnt lgkmcnt(0)
	s_barrier
	s_mov_b32 s3, 0
	v_mfma_f32_16x16x32_f16 v[132:135], v[6:9], v[124:127], v[168:171]
	v_mfma_f32_16x16x32_f16 v[136:139], v[10:13], v[124:127], v[168:171]
	v_mfma_f32_16x16x32_f16 v[140:143], v[18:21], v[124:127], v[168:171]
	s_nop 0
	v_mfma_f32_16x16x32_f16 v[132:135], v[2:5], v[128:131], v[132:135]
	s_nop 1
	v_mfma_f32_16x16x32_f16 v[136:139], v[14:17], v[128:131], v[136:139]
	s_nop 1
	v_mfma_f32_16x16x32_f16 v[140:143], v[22:25], v[128:131], v[140:143]
	s_branch .LBB3_49

.LBB3_58:
	v_mul_u32_u24_e32 v2, 48, v105
	v_lshlrev_b32_e32 v90, 2, v2
	v_mov_b32_e32 v91, 0
	s_waitcnt lgkmcnt(0)
	v_lshl_add_u64 v[2:3], s[26:27], 0, v[90:91]
	v_lshlrev_b32_e32 v10, 4, v1
	v_mov_b32_e32 v11, v91
	v_lshl_add_u64 v[2:3], v[2:3], 0, v[10:11]
	v_lshl_add_u64 v[4:5], s[30:31], 0, v[90:91]
	global_load_dwordx4 v[26:29], v10, s[28:29]
	global_load_dwordx4 v[30:33], v10, s[28:29] offset:64
	global_load_dwordx4 v[34:37], v[2:3], off
	global_load_dwordx4 v[38:41], v[2:3], off offset:64
	global_load_dwordx4 v[42:45], v[2:3], off offset:128
	global_load_dwordx4 v[46:49], v[2:3], off offset:3072
	global_load_dwordx4 v[50:53], v[2:3], off offset:3136
	global_load_dwordx4 v[54:57], v[2:3], off offset:3200
	v_lshl_add_u64 v[2:3], v[4:5], 0, v[10:11]
	global_load_dwordx4 v[58:61], v[2:3], off
	global_load_dwordx4 v[62:65], v[2:3], off offset:64
	global_load_dwordx4 v[66:69], v[2:3], off offset:128
	global_load_dwordx4 v[70:73], v[2:3], off offset:3072
	global_load_dwordx4 v[74:77], v[2:3], off offset:3136
	global_load_dwordx4 v[78:81], v[2:3], off offset:3200
	s_nop 0
	global_load_dwordx4 v[2:5], v10, s[16:17]
	global_load_dwordx4 v[6:9], v10, s[16:17] offset:64
	s_mov_b32 s12, 0x3e8293ee
	v_lshlrev_b32_e32 v11, 5, v1
	s_movk_i32 s7, 0x210
	s_mul_i32 s13, s2, 0x1040
	v_lshlrev_b32_e32 v90, 3, v1
	v_mad_u32_u24 v107, v105, s7, v11
	v_lshl_add_u64 v[98:99], s[18:19], 0, v[90:91]
	v_lshl_add_u64 v[100:101], s[20:21], 0, v[90:91]
	v_mov_b32_e32 v90, v91
	v_lshlrev_b32_e32 v106, 2, v1
	s_mov_b32 s3, 0
	s_mov_b32 s6, -3
	v_mov_b32_e32 v12, v91
	v_mov_b32_e32 v13, v91
	v_mov_b32_e32 v16, v91
	v_mov_b32_e32 v17, v91
	v_mov_b32_e32 v20, v91
	v_mov_b32_e32 v21, v91
	v_mov_b32_e32 v24, v91
	v_mov_b32_e32 v25, v91
	v_or_b32_e32 v108, s13, v105
	s_movk_i32 s7, 0x401
	v_mov_b64_e32 v[92:93], v[90:91]
	v_mov_b64_e32 v[94:95], v[90:91]
	v_mov_b64_e32 v[96:97], v[90:91]
	v_mov_b64_e32 v[102:103], v[90:91]
	s_waitcnt vmcnt(13)
	v_pk_mul_f32 v[10:11], v[34:35], s[12:13] op_sel_hi:[1,0]
	v_pk_mul_f32 v[14:15], v[36:37], s[12:13] op_sel_hi:[1,0]
	s_waitcnt vmcnt(12)
	v_pk_mul_f32 v[82:83], v[38:39], s[12:13] op_sel_hi:[1,0]
	v_pk_mul_f32 v[84:85], v[40:41], s[12:13] op_sel_hi:[1,0]
	s_waitcnt vmcnt(11)
	v_pk_mul_f32 v[86:87], v[42:43], s[12:13] op_sel_hi:[1,0]
	v_pk_mul_f32 v[88:89], v[44:45], s[12:13] op_sel_hi:[1,0]
	s_waitcnt vmcnt(10)
	v_pk_mul_f32 v[46:47], v[46:47], s[12:13] op_sel_hi:[1,0]
	v_pk_mul_f32 v[48:49], v[48:49], s[12:13] op_sel_hi:[1,0]
	s_waitcnt vmcnt(9)
	v_pk_mul_f32 v[50:51], v[50:51], s[12:13] op_sel_hi:[1,0]
	v_pk_mul_f32 v[52:53], v[52:53], s[12:13] op_sel_hi:[1,0]
	s_waitcnt vmcnt(8)
	v_pk_mul_f32 v[54:55], v[54:55], s[12:13] op_sel_hi:[1,0]
	v_pk_mul_f32 v[56:57], v[56:57], s[12:13] op_sel_hi:[1,0]
	v_pk_mul_f32 v[26:27], v[26:27], s[12:13] op_sel_hi:[1,0]
	v_pk_mul_f32 v[28:29], v[28:29], s[12:13] op_sel_hi:[1,0]
	v_pk_mul_f32 v[30:31], v[30:31], s[12:13] op_sel_hi:[1,0]
	v_pk_mul_f32 v[32:33], v[32:33], s[12:13] op_sel_hi:[1,0]
	s_waitcnt vmcnt(7)
	v_cvt_pk_f16_f32 v34, v58, v59
	v_cvt_pk_f16_f32 v35, v60, v61
	s_waitcnt vmcnt(6)
	v_cvt_pk_f16_f32 v36, v62, v63
	v_cvt_pk_f16_f32 v37, v64, v65
	s_waitcnt vmcnt(5)
	v_cvt_pk_f16_f32 v18, v66, v67
	v_cvt_pk_f16_f32 v19, v68, v69
	s_waitcnt vmcnt(4)
	v_cvt_pk_f16_f32 v38, v70, v71
	v_cvt_pk_f16_f32 v39, v72, v73
	s_waitcnt vmcnt(3)
	v_cvt_pk_f16_f32 v40, v74, v75
	v_cvt_pk_f16_f32 v41, v76, v77
	s_waitcnt vmcnt(2)
	v_cvt_pk_f16_f32 v22, v78, v79
	v_cvt_pk_f16_f32 v23, v80, v81
	v_cvt_pk_f16_f32 v42, v10, v11
	v_cvt_pk_f16_f32 v43, v14, v15
	v_cvt_pk_f16_f32 v44, v82, v83
	v_cvt_pk_f16_f32 v45, v84, v85
	v_cvt_pk_f16_f32 v10, v86, v87
	v_cvt_pk_f16_f32 v11, v88, v89
	v_cvt_pk_f16_f32 v46, v46, v47
	v_cvt_pk_f16_f32 v47, v48, v49
	v_cvt_pk_f16_f32 v48, v50, v51
	v_cvt_pk_f16_f32 v49, v52, v53
	v_cvt_pk_f16_f32 v14, v54, v55
	v_cvt_pk_f16_f32 v15, v56, v57
	v_mov_b64_e32 v[50:51], v[90:91]
	v_mov_b64_e32 v[52:53], v[90:91]
	v_mov_b64_e32 v[54:55], v[90:91]
	v_mov_b64_e32 v[56:57], v[90:91]
	v_mov_b64_e32 v[58:59], v[90:91]
	v_mov_b64_e32 v[60:61], v[90:91]
	v_mov_b64_e32 v[62:63], v[90:91]
	v_mov_b64_e32 v[64:65], v[90:91]
	v_mov_b64_e32 v[66:67], v[90:91]
	v_mov_b64_e32 v[68:69], v[90:91]
	v_mov_b64_e32 v[70:71], v[90:91]
	v_mov_b64_e32 v[72:73], v[90:91]
	v_mov_b64_e32 v[74:75], v[90:91]
	v_mov_b64_e32 v[76:77], v[90:91]
	v_mov_b64_e32 v[78:79], v[90:91]
	v_mov_b64_e32 v[80:81], v[90:91]
	v_mov_b64_e32 v[82:83], v[90:91]
	v_mov_b64_e32 v[84:85], v[90:91]
	v_mov_b64_e32 v[86:87], v[90:91]
	v_mov_b64_e32 v[88:89], v[90:91]
	s_waitcnt vmcnt(0)
	s_barrier
	s_branch .LBB3_60

.LBB3_159:
	v_lshlrev_b32_e32 v14, 4, v1
	v_lshlrev_b32_e32 v34, 8, v105
	v_or_b32_e32 v35, v14, v34
	s_waitcnt lgkmcnt(0)
	global_load_dwordx4 v[2:5], v14, s[10:11]
	global_load_dwordx4 v[6:9], v14, s[10:11] offset:64
	global_load_dwordx4 v[10:13], v14, s[10:11] offset:128
	s_nop 0
	global_load_dwordx4 v[14:17], v35, s[8:9]
	global_load_dwordx4 v[18:21], v35, s[8:9] offset:64
	global_load_dwordx4 v[22:25], v35, s[8:9] offset:128
	global_load_dwordx4 v[26:29], v35, s[8:9] offset:192
	v_or_b32_e32 v36, 0x1000, v35
	v_or_b32_e32 v35, 0x2000, v35
	global_load_dwordx4 v[30:33], v36, s[8:9]
	global_load_dwordx4 v[38:41], v36, s[8:9] offset:64
	global_load_dwordx4 v[42:45], v36, s[8:9] offset:128
	global_load_dwordx4 v[46:49], v36, s[8:9] offset:192
	global_load_dwordx4 v[50:53], v35, s[8:9]
	global_load_dwordx4 v[54:57], v35, s[8:9] offset:64
	global_load_dwordx4 v[58:61], v35, s[8:9] offset:128
	global_load_dwordx4 v[62:65], v35, s[8:9] offset:192
	s_mov_b32 s6, 0x4038aa3b
	v_mul_u32_u24_e32 v35, 0x210, v105
	v_lshlrev_b32_e32 v1, 5, v1
	s_movk_i32 s5, 0x210
	v_and_b32_e32 v37, 48, v0
	v_add_u32_e32 v36, v35, v1
	v_mad_u32_u24 v66, v105, s5, v34
	s_mov_b32 s4, -1
	v_add_u32_e32 v37, v66, v37
	s_waitcnt vmcnt(14)
	v_pk_mul_f32 v[0:1], v[2:3], s[6:7] op_sel_hi:[1,0]
	v_pk_mul_f32 v[2:3], v[4:5], s[6:7] op_sel_hi:[1,0]
	s_waitcnt vmcnt(13)
	v_pk_mul_f32 v[4:5], v[6:7], s[6:7] op_sel_hi:[1,0]
	v_pk_mul_f32 v[6:7], v[8:9], s[6:7] op_sel_hi:[1,0]
	s_waitcnt vmcnt(12)
	v_pk_mul_f32 v[8:9], v[10:11], s[6:7] op_sel_hi:[1,0]
	v_pk_mul_f32 v[10:11], v[12:13], s[6:7] op_sel_hi:[1,0]
	s_waitcnt vmcnt(11)
	v_pk_mul_f32 v[12:13], v[14:15], s[6:7] op_sel_hi:[1,0]
	v_pk_mul_f32 v[14:15], v[16:17], s[6:7] op_sel_hi:[1,0]
	s_waitcnt vmcnt(10)
	v_pk_mul_f32 v[16:17], v[18:19], s[6:7] op_sel_hi:[1,0]
	v_pk_mul_f32 v[18:19], v[20:21], s[6:7] op_sel_hi:[1,0]
	s_waitcnt vmcnt(9)
	v_pk_mul_f32 v[20:21], v[22:23], s[6:7] op_sel_hi:[1,0]
	v_pk_mul_f32 v[22:23], v[24:25], s[6:7] op_sel_hi:[1,0]
	s_waitcnt vmcnt(8)
	v_pk_mul_f32 v[24:25], v[26:27], s[6:7] op_sel_hi:[1,0]
	v_pk_mul_f32 v[26:27], v[28:29], s[6:7] op_sel_hi:[1,0]
	v_cvt_pk_f16_f32 v12, v12, v13
	v_cvt_pk_f16_f32 v13, v14, v15
	v_cvt_pk_f16_f32 v14, v16, v17
	v_cvt_pk_f16_f32 v15, v18, v19
	v_cvt_pk_f16_f32 v16, v20, v21
	v_cvt_pk_f16_f32 v17, v22, v23
	v_cvt_pk_f16_f32 v18, v24, v25
	v_cvt_pk_f16_f32 v19, v26, v27
	s_waitcnt vmcnt(7)
	v_pk_mul_f32 v[20:21], v[30:31], s[6:7] op_sel_hi:[1,0]
	v_pk_mul_f32 v[22:23], v[32:33], s[6:7] op_sel_hi:[1,0]
	s_waitcnt vmcnt(6)
	v_pk_mul_f32 v[24:25], v[38:39], s[6:7] op_sel_hi:[1,0]
	v_pk_mul_f32 v[26:27], v[40:41], s[6:7] op_sel_hi:[1,0]
	s_waitcnt vmcnt(5)
	v_pk_mul_f32 v[28:29], v[42:43], s[6:7] op_sel_hi:[1,0]
	v_pk_mul_f32 v[30:31], v[44:45], s[6:7] op_sel_hi:[1,0]
	s_waitcnt vmcnt(4)
	v_pk_mul_f32 v[32:33], v[46:47], s[6:7] op_sel_hi:[1,0]
	v_pk_mul_f32 v[34:35], v[48:49], s[6:7] op_sel_hi:[1,0]
	s_waitcnt vmcnt(3)
	v_pk_mul_f32 v[38:39], v[50:51], s[6:7] op_sel_hi:[1,0]
	v_pk_mul_f32 v[40:41], v[52:53], s[6:7] op_sel_hi:[1,0]
	s_waitcnt vmcnt(2)
	v_pk_mul_f32 v[42:43], v[54:55], s[6:7] op_sel_hi:[1,0]
	v_pk_mul_f32 v[44:45], v[56:57], s[6:7] op_sel_hi:[1,0]
	s_waitcnt vmcnt(1)
	v_pk_mul_f32 v[46:47], v[58:59], s[6:7] op_sel_hi:[1,0]
	v_pk_mul_f32 v[48:49], v[60:61], s[6:7] op_sel_hi:[1,0]
	s_waitcnt vmcnt(0)
	v_pk_mul_f32 v[50:51], v[62:63], s[6:7] op_sel_hi:[1,0]
	v_pk_mul_f32 v[52:53], v[64:65], s[6:7] op_sel_hi:[1,0]
	v_cvt_pk_f16_f32 v20, v20, v21
	v_cvt_pk_f16_f32 v21, v22, v23
	v_cvt_pk_f16_f32 v22, v24, v25
	v_cvt_pk_f16_f32 v23, v26, v27
	v_cvt_pk_f16_f32 v24, v28, v29
	v_cvt_pk_f16_f32 v25, v30, v31
	v_cvt_pk_f16_f32 v26, v32, v33
	v_cvt_pk_f16_f32 v27, v34, v35
	v_cvt_pk_f16_f32 v28, v38, v39
	v_cvt_pk_f16_f32 v29, v40, v41
	v_cvt_pk_f16_f32 v30, v42, v43
	v_cvt_pk_f16_f32 v31, v44, v45
	v_cvt_pk_f16_f32 v32, v46, v47
	v_cvt_pk_f16_f32 v33, v48, v49
	v_cvt_pk_f16_f32 v34, v50, v51
	v_cvt_pk_f16_f32 v35, v52, v53
	s_barrier
	s_branch .LBB3_161

.LBB3_166:
	s_waitcnt lgkmcnt(0)
	s_andn2_saveexec_b64 s[8:9], s[38:39]
	s_cbranch_execz .LBB3_175
	s_load_dwordx4 s[4:7], s[0:1], 0xa8
	s_load_dwordx2 s[2:3], s[0:1], 0xb8
	v_lshrrev_b32_e32 v29, 2, v0
	v_lshlrev_b32_e32 v49, 6, v0
	v_and_b32_e32 v41, 12, v29
	v_and_b32_e32 v45, 0x3c0, v49
	v_or_b32_e32 v53, 3, v29
	v_or_b32_e32 v2, v41, v45
	v_or_b32_e32 v5, v53, v45
	v_lshlrev_b32_e32 v21, 2, v2
	v_lshlrev_b32_e32 v13, 2, v5
	v_or_b32_e32 v89, 19, v29
	s_waitcnt lgkmcnt(0)
	global_load_dwordx3 v[2:4], v21, s[4:5]
	global_load_dwordx3 v[6:8], v21, s[6:7]
	global_load_dword v5, v13, s[4:5]
	global_load_dword v9, v13, s[6:7]
	global_load_dwordx3 v[10:12], v21, s[4:5] offset:64
	global_load_dwordx3 v[14:16], v21, s[6:7] offset:64
	v_or_b32_e32 v13, v89, v45
	v_lshlrev_b32_e32 v25, 2, v13
	v_or_b32_e32 v93, 35, v29
	v_or_b32_e32 v61, 0x400, v45
	global_load_dword v13, v25, s[4:5]
	global_load_dword v17, v25, s[6:7]
	global_load_dwordx3 v[18:20], v21, s[4:5] offset:128
	global_load_dwordx3 v[22:24], v21, s[6:7] offset:128
	v_or_b32_e32 v25, v93, v45
	global_load_dwordx3 v[26:28], v21, s[4:5] offset:192
	global_load_dwordx3 v[30:32], v21, s[6:7] offset:192
	v_or_b32_e32 v21, v61, v41
	v_lshlrev_b32_e32 v62, 2, v21
	v_lshlrev_b32_e32 v33, 2, v25
	global_load_dwordx3 v[34:36], v62, s[4:5] offset:64
	global_load_dwordx3 v[42:44], v62, s[6:7] offset:64
	global_load_dword v21, v33, s[4:5]
	global_load_dword v25, v33, s[6:7]
	v_or_b32_e32 v81, 51, v29
	v_or_b32_e32 v29, v81, v45
	v_lshlrev_b32_e32 v37, 2, v29
	global_load_dword v29, v37, s[4:5]
	global_load_dword v33, v37, s[6:7]
	v_or_b32_e32 v37, v61, v89
	v_lshlrev_b32_e32 v38, 2, v37
	global_load_dword v37, v38, s[4:5]
	global_load_dword v39, v38, s[6:7]
	global_load_dwordx3 v[46:48], v62, s[4:5] offset:128
	global_load_dwordx3 v[50:52], v62, s[6:7] offset:128
	v_or_b32_e32 v38, v61, v93
	v_lshlrev_b32_e32 v38, 2, v38
	global_load_dword v63, v38, s[4:5]
	global_load_dword v95, v38, s[6:7]
	global_load_dwordx3 v[54:56], v62, s[4:5] offset:192
	global_load_dwordx3 v[58:60], v62, s[6:7] offset:192
	s_mov_b32 s0, 0x4038aa3b
	s_mov_b32 s10, 0x3f2aaaab
	s_mov_b32 s11, 0x3f317218
	v_or_b32_e32 v40, s34, v65
	v_lshlrev_b32_e32 v118, 6, v64
	v_lshlrev_b32_e32 v65, 7, v65
	s_waitcnt vmcnt(24)
	v_pk_mul_f32 v[2:3], v[2:3], v[6:7]
	s_waitcnt vmcnt(20)
	v_pk_mul_f32 v[6:7], v[10:11], v[14:15]
	v_pk_mul_f32 v[4:5], v[4:5], v[8:9]
	v_pk_mul_f32 v[6:7], v[6:7], s[0:1] op_sel_hi:[1,0]
	s_waitcnt vmcnt(18)
	v_pk_mul_f32 v[8:9], v[12:13], v[16:17]
	v_pk_mul_f32 v[2:3], v[2:3], s[0:1] op_sel_hi:[1,0]
	s_waitcnt vmcnt(16)
	v_pk_mul_f32 v[10:11], v[18:19], v[22:23]
	v_pk_mul_f32 v[22:23], v[8:9], s[0:1] op_sel_hi:[1,0]
	v_pk_mul_f32 v[10:11], v[10:11], s[0:1] op_sel_hi:[1,0]
	s_waitcnt vmcnt(14)
	v_pk_mul_f32 v[14:15], v[26:27], v[30:31]
	v_cvt_pk_f16_f32 v2, v2, v3
	v_pk_mul_f32 v[14:15], v[14:15], s[0:1] op_sel_hi:[1,0]
	s_waitcnt vmcnt(12)
	v_pk_mul_f32 v[18:19], v[34:35], v[42:43]
	s_waitcnt vmcnt(10)
	v_pk_mul_f32 v[12:13], v[20:21], v[24:25]
	v_pk_mul_f32 v[20:21], v[4:5], s[0:1] op_sel_hi:[1,0]
	v_cvt_pk_f16_f32 v4, v6, v7
	v_cvt_pk_f16_f32 v6, v10, v11
	v_pk_mul_f32 v[10:11], v[12:13], s[0:1] op_sel_hi:[1,0]
	s_waitcnt vmcnt(8)
	v_pk_mul_f32 v[16:17], v[28:29], v[32:33]
	v_cvt_pk_f16_f32 v7, v10, v11
	v_or_b32_e32 v10, v61, v81
	v_or_b32_e32 v11, v61, v53
	v_pk_mul_f32 v[18:19], v[18:19], s[0:1] op_sel_hi:[1,0]
	v_cvt_pk_f16_f32 v8, v14, v15
	v_lshlrev_b32_e32 v10, 2, v10
	v_lshlrev_b32_e32 v11, 2, v11
	v_or_b32_e32 v14, 0x800, v45
	v_pk_mul_f32 v[12:13], v[16:17], s[0:1] op_sel_hi:[1,0]
	v_cvt_pk_f16_f32 v3, v20, v21
	v_cvt_pk_f16_f32 v5, v22, v23
	global_load_dword v33, v10, s[4:5]
	global_load_dword v57, v10, s[6:7]
	v_cvt_pk_f16_f32 v10, v18, v19
	v_mov_b32_e32 v38, v44
	global_load_dwordx3 v[16:18], v62, s[4:5]
	global_load_dwordx3 v[20:22], v62, s[6:7]
	global_load_dword v19, v11, s[4:5]
	global_load_dword v23, v11, s[6:7]
	v_or_b32_e32 v11, v14, v41
	v_cvt_pk_f16_f32 v9, v12, v13
	s_waitcnt vmcnt(12)
	v_pk_mul_f32 v[12:13], v[36:37], v[38:39]
	v_lshlrev_b32_e32 v15, 2, v11
	v_or_b32_e32 v11, v14, v93
	v_pk_mul_f32 v[12:13], v[12:13], s[0:1] op_sel_hi:[1,0]
	v_lshlrev_b32_e32 v11, 2, v11
	global_load_dwordx3 v[24:26], v15, s[4:5] offset:128
	global_load_dwordx3 v[28:30], v15, s[6:7] offset:128
	global_load_dword v27, v11, s[4:5]
	global_load_dword v31, v11, s[6:7]
	v_cvt_pk_f16_f32 v11, v12, v13
	s_waitcnt vmcnt(14)
	v_pk_mul_f32 v[12:13], v[46:47], v[50:51]
	v_or_b32_e32 v32, v14, v81
	v_pk_mul_f32 v[12:13], v[12:13], s[0:1] op_sel_hi:[1,0]
	global_load_dwordx3 v[42:44], v15, s[4:5] offset:192
	global_load_dwordx3 v[66:68], v15, s[6:7] offset:192
	v_lshlrev_b32_e32 v32, 2, v32
	v_cvt_pk_f16_f32 v12, v12, v13
	v_or_b32_e32 v13, v14, v53
	global_load_dword v39, v32, s[4:5]
	global_load_dword v45, v32, s[6:7]
	v_lshlrev_b32_e32 v13, 2, v13
	global_load_dwordx3 v[70:72], v15, s[4:5]
	global_load_dwordx3 v[74:76], v15, s[6:7]
	global_load_dword v61, v13, s[4:5]
	global_load_dword v69, v13, s[6:7]
	global_load_dwordx3 v[78:80], v15, s[4:5] offset:64
	global_load_dwordx3 v[82:84], v15, s[6:7] offset:64
	v_or_b32_e32 v13, v14, v89
	v_lshlrev_b32_e32 v13, 2, v13
	v_or_b32_e32 v38, 0xc00, v49
	global_load_dword v73, v13, s[4:5]
	global_load_dword v77, v13, s[6:7]
	v_or_b32_e32 v13, v41, v38
	v_lshlrev_b32_e32 v32, 2, v13
	v_or_b32_e32 v13, v81, v38
	global_load_dwordx3 v[86:88], v32, s[4:5] offset:192
	global_load_dwordx3 v[90:92], v32, s[6:7] offset:192
	v_mov_b32_e32 v62, v48
	v_lshlrev_b32_e32 v13, 2, v13
	v_mov_b32_e32 v94, v52
	global_load_dword v81, v13, s[4:5]
	global_load_dword v85, v13, s[6:7]
	s_waitcnt vmcnt(28)
	v_pk_mul_f32 v[14:15], v[62:63], v[94:95]
	v_or_b32_e32 v13, v53, v38
	v_lshlrev_b32_e32 v13, 2, v13
	v_pk_mul_f32 v[14:15], v[14:15], s[0:1] op_sel_hi:[1,0]
	global_load_dwordx3 v[46:48], v32, s[4:5]
	global_load_dwordx3 v[50:52], v32, s[6:7]
	global_load_dword v49, v13, s[4:5]
	global_load_dword v53, v13, s[6:7]
	v_cvt_pk_f16_f32 v13, v14, v15
	v_or_b32_e32 v14, v89, v38
	global_load_dwordx3 v[94:96], v32, s[4:5] offset:64
	global_load_dwordx3 v[98:100], v32, s[6:7] offset:64
	v_lshlrev_b32_e32 v14, 2, v14
	global_load_dword v63, v14, s[4:5]
	global_load_dword v89, v14, s[6:7]
	global_load_dwordx3 v[102:104], v32, s[4:5] offset:128
	global_load_dwordx3 v[106:108], v32, s[6:7] offset:128
	v_lshlrev_b32_e32 v32, 4, v0
	v_and_or_b32 v32, v32, 48, v41
	v_lshlrev_b32_e32 v32, 2, v32
	global_load_dwordx4 v[34:37], v32, s[2:3]
	s_waitcnt vmcnt(37)
	v_pk_mul_f32 v[14:15], v[54:55], v[58:59]
	v_mov_b32_e32 v32, v56
	v_pk_mul_f32 v[14:15], v[14:15], s[0:1] op_sel_hi:[1,0]
	v_mov_b32_e32 v56, v60
	v_cvt_pk_f16_f32 v14, v14, v15
	v_or_b32_e32 v15, v93, v38
	v_lshlrev_b32_e32 v15, 2, v15
	s_mov_b32 s2, 0xc2ce8ed0
	s_mov_b32 s3, 0x42b17218
	v_and_b32_e32 v0, 48, v0
	s_waitcnt vmcnt(35)
	v_pk_mul_f32 v[32:33], v[32:33], v[56:57]
	global_load_dword v55, v15, s[4:5]
	global_load_dword v57, v15, s[6:7]
	v_pk_mul_f32 v[32:33], v[32:33], s[0:1] op_sel_hi:[1,0]
	s_waitcnt vmcnt(35)
	v_pk_mul_f32 v[16:17], v[16:17], v[20:21]
	s_waitcnt vmcnt(33)
	v_pk_mul_f32 v[18:19], v[18:19], v[22:23]
	v_pk_mul_f32 v[16:17], v[16:17], s[0:1] op_sel_hi:[1,0]
	v_pk_mul_f32 v[18:19], v[18:19], s[0:1] op_sel_hi:[1,0]
	v_cvt_pk_f16_f32 v16, v16, v17
	v_cvt_pk_f16_f32 v17, v18, v19
	v_cvt_pk_f16_f32 v15, v32, v33
	s_mov_b32 s4, 0x7f800000
	s_mov_b32 s6, 0x33800000
	s_waitcnt vmcnt(31)
	v_pk_mul_f32 v[18:19], v[24:25], v[28:29]
	s_waitcnt vmcnt(29)
	v_pk_mul_f32 v[20:21], v[26:27], v[30:31]
	v_pk_mul_f32 v[18:19], v[18:19], s[0:1] op_sel_hi:[1,0]
	v_pk_mul_f32 v[20:21], v[20:21], s[0:1] op_sel_hi:[1,0]
	v_cvt_pk_f16_f32 v18, v18, v19
	s_waitcnt vmcnt(28)
	v_mov_b32_e32 v38, v44
	s_waitcnt vmcnt(27)
	v_mov_b32_e32 v44, v68
	v_cvt_pk_f16_f32 v19, v20, v21
	v_pk_mul_f32 v[20:21], v[42:43], v[66:67]
	s_mov_b32 s7, 0x3c23d70a
	s_waitcnt vmcnt(25)
	v_pk_mul_f32 v[22:23], v[38:39], v[44:45]
	v_pk_mul_f32 v[20:21], v[20:21], s[0:1] op_sel_hi:[1,0]
	v_pk_mul_f32 v[22:23], v[22:23], s[0:1] op_sel_hi:[1,0]
	s_waitcnt vmcnt(24)
	v_mov_b32_e32 v60, v72
	s_waitcnt vmcnt(23)
	v_mov_b32_e32 v68, v76
	v_cvt_pk_f16_f32 v20, v20, v21
	v_cvt_pk_f16_f32 v21, v22, v23
	v_pk_mul_f32 v[22:23], v[70:71], v[74:75]
	s_waitcnt vmcnt(21)
	v_pk_mul_f32 v[24:25], v[60:61], v[68:69]
	v_pk_mul_f32 v[22:23], v[22:23], s[0:1] op_sel_hi:[1,0]
	v_pk_mul_f32 v[24:25], v[24:25], s[0:1] op_sel_hi:[1,0]
	s_waitcnt vmcnt(20)
	v_mov_b32_e32 v72, v80
	s_waitcnt vmcnt(19)
	v_mov_b32_e32 v76, v84
	v_cvt_pk_f16_f32 v22, v22, v23
	v_cvt_pk_f16_f32 v23, v24, v25
	v_pk_mul_f32 v[24:25], v[78:79], v[82:83]
	s_waitcnt vmcnt(17)
	v_pk_mul_f32 v[26:27], v[72:73], v[76:77]
	v_pk_mul_f32 v[24:25], v[24:25], s[0:1] op_sel_hi:[1,0]
	v_pk_mul_f32 v[26:27], v[26:27], s[0:1] op_sel_hi:[1,0]
	s_waitcnt vmcnt(16)
	v_mov_b32_e32 v80, v88
	s_waitcnt vmcnt(15)
	v_mov_b32_e32 v84, v92
	v_cvt_pk_f16_f32 v24, v24, v25
	v_cvt_pk_f16_f32 v25, v26, v27
	v_pk_mul_f32 v[26:27], v[86:87], v[90:91]
	s_waitcnt vmcnt(13)
	v_pk_mul_f32 v[28:29], v[80:81], v[84:85]
	v_pk_mul_f32 v[26:27], v[26:27], s[0:1] op_sel_hi:[1,0]
	v_pk_mul_f32 v[28:29], v[28:29], s[0:1] op_sel_hi:[1,0]
	v_cvt_pk_f16_f32 v26, v26, v27
	v_cvt_pk_f16_f32 v27, v28, v29
	s_waitcnt vmcnt(11)
	v_pk_mul_f32 v[28:29], v[46:47], v[50:51]
	s_waitcnt vmcnt(9)
	v_pk_mul_f32 v[30:31], v[48:49], v[52:53]
	v_pk_mul_f32 v[28:29], v[28:29], s[0:1] op_sel_hi:[1,0]
	v_pk_mul_f32 v[30:31], v[30:31], s[0:1] op_sel_hi:[1,0]
	s_waitcnt vmcnt(8)
	v_mov_b32_e32 v62, v96
	s_waitcnt vmcnt(7)
	v_mov_b32_e32 v88, v100
	v_cvt_pk_f16_f32 v28, v28, v29
	v_cvt_pk_f16_f32 v29, v30, v31
	v_pk_mul_f32 v[30:31], v[94:95], v[98:99]
	s_waitcnt vmcnt(5)
	v_pk_mul_f32 v[32:33], v[62:63], v[88:89]
	v_pk_mul_f32 v[30:31], v[30:31], s[0:1] op_sel_hi:[1,0]
	v_pk_mul_f32 v[32:33], v[32:33], s[0:1] op_sel_hi:[1,0]
	v_cvt_pk_f16_f32 v30, v30, v31
	v_cvt_pk_f16_f32 v31, v32, v33
	s_waitcnt vmcnt(3)
	v_pk_mul_f32 v[32:33], v[102:103], v[106:107]
	s_waitcnt vmcnt(2)
	v_cmp_ngt_f32_e32 vcc, s2, v34
	v_pk_mul_f32 v[32:33], v[32:33], s[0:1] op_sel_hi:[1,0]
	s_mov_b32 s1, 0x3fb8aa3b
	v_cvt_pk_f16_f32 v32, v32, v33
	v_mul_f32_e32 v33, 0x3fb8aa3b, v34
	v_fma_f32 v38, v34, s1, -v33
	v_rndne_f32_e32 v39, v33
	v_fmac_f32_e32 v38, 0x32a5705f, v34
	v_sub_f32_e32 v33, v33, v39
	v_add_f32_e32 v33, v33, v38
	v_exp_f32_e32 v33, v33
	v_cvt_i32_f32_e32 v38, v39
	v_mov_b32_e32 v107, 0x7f800000
	v_mov_b32_e32 v54, v104
	v_mov_b32_e32 v56, v108
	v_ldexp_f32 v33, v33, v38
	v_cndmask_b32_e32 v33, 0, v33, vcc
	v_cmp_nlt_f32_e32 vcc, s3, v34
	s_waitcnt vmcnt(0)
	v_pk_mul_f32 v[42:43], v[54:55], v[56:57]
	v_mov_b32_e32 v103, 0x41200000
	v_cndmask_b32_e32 v33, v107, v33, vcc
	v_add_f32_e32 v34, 1.0, v33
	v_add_f32_e32 v38, -1.0, v34
	v_sub_f32_e32 v39, v38, v34
	v_add_f32_e32 v39, 1.0, v39
	v_sub_f32_e32 v38, v33, v38
	v_add_f32_e32 v41, v38, v39
	v_frexp_mant_f32_e32 v44, v34
	v_cvt_f64_f32_e32 v[38:39], v34
	v_frexp_exp_i32_f64_e32 v38, v[38:39]
	v_cmp_gt_f32_e32 vcc, s10, v44
	s_mov_b32 s5, 0xbd23d70a
	v_pk_mul_f32 v[42:43], v[42:43], s[0:1] op_sel_hi:[1,0]
	v_subbrev_co_u32_e32 v50, vcc, 0, v38, vcc
	v_sub_u32_e32 v38, 0, v50
	v_ldexp_f32 v34, v34, v38
	v_ldexp_f32 v38, v41, v38
	v_add_f32_e32 v41, -1.0, v34
	v_add_f32_e32 v39, 1.0, v41
	v_sub_f32_e32 v39, v34, v39
	v_add_f32_e32 v44, v38, v39
	v_add_f32_e32 v39, 1.0, v34
	v_add_f32_e32 v45, -1.0, v39
	v_sub_f32_e32 v34, v34, v45
	v_add_f32_e32 v34, v38, v34
	v_add_f32_e32 v51, v39, v34
	v_rcp_f32_e32 v52, v51
	v_sub_f32_e32 v38, v39, v51
	v_add_f32_e32 v39, v41, v44
	v_add_f32_e32 v34, v34, v38
	v_sub_f32_e32 v38, v41, v39
	v_mul_f32_e32 v53, v39, v52
	v_add_f32_e32 v41, v44, v38
	v_mul_f32_e32 v44, v51, v53
	v_fma_f32 v46, v53, v51, -v44
	v_fmac_f32_e32 v46, v53, v34
	v_add_f32_e32 v38, v44, v46
	v_sub_f32_e32 v45, v39, v38
	v_pk_add_f32 v[48:49], v[38:39], v[44:45] neg_lo:[0,1] neg_hi:[0,1]
	v_mov_b32_e32 v47, v38
	v_pk_add_f32 v[38:39], v[48:49], v[46:47] neg_lo:[0,1] neg_hi:[0,1]
	v_cmp_neq_f32_e32 vcc, s4, v33
	v_add_f32_e32 v39, v41, v39
	v_add_f32_e32 v38, v38, v39
	v_add_f32_e32 v39, v45, v38
	v_mul_f32_e32 v41, v52, v39
	v_mul_f32_e32 v44, v51, v41
	v_fma_f32 v46, v41, v51, -v44
	v_fmac_f32_e32 v46, v41, v34
	v_sub_f32_e32 v34, v45, v39
	v_add_f32_e32 v34, v38, v34
	v_add_f32_e32 v38, v44, v46
	v_sub_f32_e32 v45, v39, v38
	v_pk_add_f32 v[48:49], v[38:39], v[44:45] neg_lo:[0,1] neg_hi:[0,1]
	v_mov_b32_e32 v47, v38
	v_pk_add_f32 v[38:39], v[48:49], v[46:47] neg_lo:[0,1] neg_hi:[0,1]
	v_cvt_f32_i32_e32 v44, v50
	v_add_f32_e32 v34, v34, v39
	v_add_f32_e32 v34, v38, v34
	v_add_f32_e32 v38, v53, v41
	v_add_f32_e32 v34, v45, v34
	v_sub_f32_e32 v39, v38, v53
	v_mul_f32_e32 v34, v52, v34
	v_sub_f32_e32 v39, v41, v39
	v_add_f32_e32 v41, v39, v34
	v_add_f32_e32 v45, v38, v41
	v_mul_f32_e32 v46, v45, v45
	v_mov_b32_e32 v34, 0x3ecc95a3
	v_sub_f32_e32 v38, v45, v38
	v_fmamk_f32 v39, v46, 0x3e9b6dac, v34
	v_sub_f32_e32 v38, v41, v38
	v_fmaak_f32 v39, v46, v39, 0x3f2aaada
	v_ldexp_f32 v47, v45, 1
	v_ldexp_f32 v41, v38, 1
	v_mul_f32_e32 v45, v45, v46
	v_mov_b32_e32 v38, 0x3f317218
	v_pk_mul_f32 v[48:49], v[44:45], v[38:39]
	s_mov_b32 s0, 0x42000
	v_fma_f32 v46, v44, s11, -v48
	v_fmac_f32_e32 v46, 0xb102e308, v44
	v_pk_add_f32 v[44:45], v[48:49], v[46:47]
	v_mov_b32_e32 v50, v48
	v_sub_f32_e32 v39, v45, v47
	v_sub_f32_e32 v39, v49, v39
	v_add_f32_e32 v51, v41, v39
	v_pk_add_f32 v[48:49], v[44:45], v[48:49] neg_lo:[0,1] neg_hi:[0,1]
	v_pk_add_f32 v[52:53], v[44:45], v[50:51]
	v_mov_b32_e32 v47, v44
	v_mov_b32_e32 v49, v53
	v_pk_add_f32 v[54:55], v[46:47], v[48:49] neg_lo:[0,1] neg_hi:[0,1]
	v_pk_add_f32 v[46:47], v[46:47], v[48:49]
	v_mov_b32_e32 v50, v51
	v_pk_add_f32 v[48:49], v[46:47], v[44:45] op_sel:[1,0] op_sel_hi:[0,1] neg_lo:[0,1] neg_hi:[0,1]
	v_pk_add_f32 v[56:57], v[52:53], v[48:49] op_sel_hi:[1,0] neg_lo:[0,1] neg_hi:[0,1]
	v_mov_b32_e32 v52, v53
	v_mov_b32_e32 v53, v47
	v_pk_mov_b32 v[48:49], v[44:45], v[48:49] op_sel:[1,0]
	v_mov_b32_e32 v51, v44
	v_pk_add_f32 v[48:49], v[52:53], v[48:49] neg_lo:[0,1] neg_hi:[0,1]
	v_mov_b32_e32 v56, v54
	v_pk_add_f32 v[44:45], v[50:51], v[48:49] neg_lo:[0,1] neg_hi:[0,1]
	v_mov_b32_e32 v55, v47
	v_pk_add_f32 v[48:49], v[56:57], v[44:45]
	v_mov_b32_e32 v56, 0x3f2aaada
	v_pk_add_f32 v[50:51], v[48:49], v[48:49] op_sel:[0,1] op_sel_hi:[1,0]
	v_mov_b32_e32 v63, 0
	v_pk_add_f32 v[46:47], v[46:47], v[50:51] op_sel:[1,0] op_sel_hi:[0,1]
	v_mov_b32_e32 v49, v46
	v_pk_add_f32 v[52:53], v[48:49], v[54:55] neg_lo:[0,1] neg_hi:[0,1]
	v_mov_b32_e32 v45, v50
	v_sub_f32_e32 v39, v48, v52
	v_pk_add_f32 v[44:45], v[44:45], v[52:53] neg_lo:[0,1] neg_hi:[0,1]
	v_sub_f32_e32 v39, v54, v39
	v_add_f32_e32 v39, v44, v39
	v_add_f32_e32 v39, v39, v45
	v_add_f32_e32 v39, v46, v39
	v_cndmask_b32_e32 v39, v107, v39, vcc
	v_cmp_lt_f32_e64 vcc, |v33|, s6
	v_mul_lo_u32 v62, v40, s0
	v_mov_b32_e32 v119, v63
	v_cndmask_b32_e32 v33, v39, v33, vcc
	v_add_f32_e32 v33, 0x358637bd, v33
	v_med3_f32 v39, v33, s7, v103
	v_div_scale_f32 v41, s[12:13], v39, v39, s5
	v_rcp_f32_e32 v44, v41
	v_cvt_pk_f16_f32 v33, v42, v43
	s_mov_b32 s12, 0
	v_fma_f32 v42, -v41, v44, 1.0
	v_fmac_f32_e32 v44, v42, v44
	v_div_scale_f32 v42, vcc, s5, v39, s5
	v_mul_f32_e32 v43, v42, v44
	v_fma_f32 v45, -v41, v43, v42
	v_fmac_f32_e32 v43, v45, v44
	v_fma_f32 v41, -v41, v43, v42
	v_div_fmas_f32 v41, v41, v44, v43
	v_div_fixup_f32 v41, v41, v39, s5
	v_mul_f32_e32 v39, 0x3fb8aa3b, v41
	v_fma_f32 v42, v41, s1, -v39
	v_rndne_f32_e32 v43, v39
	v_fmac_f32_e32 v42, 0x32a5705f, v41
	v_sub_f32_e32 v39, v39, v43
	v_add_f32_e32 v39, v39, v42
	v_cvt_i32_f32_e32 v42, v43
	v_mul_f32_e32 v43, 0x3fb8aa3b, v35
	v_fma_f32 v44, v35, s1, -v43
	v_rndne_f32_e32 v45, v43
	v_fmac_f32_e32 v44, 0x32a5705f, v35
	v_sub_f32_e32 v43, v43, v45
	v_add_f32_e32 v43, v43, v44
	v_exp_f32_e32 v39, v39
	v_exp_f32_e32 v43, v43
	v_cvt_i32_f32_e32 v44, v45
	v_cmp_ngt_f32_e32 vcc, s2, v35
	v_ldexp_f32 v57, v39, v42
	v_ldexp_f32 v39, v43, v44
	v_cndmask_b32_e32 v39, 0, v39, vcc
	v_cmp_nlt_f32_e32 vcc, s3, v35
	s_nop 1
	v_cndmask_b32_e32 v35, v107, v39, vcc
	v_add_f32_e32 v39, 1.0, v35
	v_add_f32_e32 v42, -1.0, v39
	v_sub_f32_e32 v43, v42, v39
	v_add_f32_e32 v43, 1.0, v43
	v_sub_f32_e32 v42, v35, v42
	v_add_f32_e32 v44, v42, v43
	v_frexp_mant_f32_e32 v45, v39
	v_cvt_f64_f32_e32 v[42:43], v39
	v_frexp_exp_i32_f64_e32 v42, v[42:43]
	v_cmp_gt_f32_e32 vcc, s10, v45
	s_nop 1
	v_subbrev_co_u32_e32 v50, vcc, 0, v42, vcc
	v_sub_u32_e32 v42, 0, v50
	v_ldexp_f32 v39, v39, v42
	v_ldexp_f32 v42, v44, v42
	v_add_f32_e32 v44, -1.0, v39
	v_add_f32_e32 v43, 1.0, v44
	v_sub_f32_e32 v43, v39, v43
	v_add_f32_e32 v45, v42, v43
	v_add_f32_e32 v43, 1.0, v39
	v_add_f32_e32 v46, -1.0, v43
	v_sub_f32_e32 v39, v39, v46
	v_add_f32_e32 v39, v42, v39
	v_add_f32_e32 v51, v43, v39
	v_rcp_f32_e32 v52, v51
	v_sub_f32_e32 v42, v43, v51
	v_add_f32_e32 v43, v44, v45
	v_add_f32_e32 v39, v39, v42
	v_mul_f32_e32 v54, v43, v52
	v_sub_f32_e32 v42, v44, v43
	v_mul_f32_e32 v44, v51, v54
	v_fma_f32 v46, v54, v51, -v44
	v_fmac_f32_e32 v46, v54, v39
	v_add_f32_e32 v53, v45, v42
	v_add_f32_e32 v42, v44, v46
	v_sub_f32_e32 v45, v43, v42
	v_pk_add_f32 v[48:49], v[42:43], v[44:45] neg_lo:[0,1] neg_hi:[0,1]
	v_mov_b32_e32 v47, v42
	v_pk_add_f32 v[42:43], v[48:49], v[46:47] neg_lo:[0,1] neg_hi:[0,1]
	v_cmp_neq_f32_e32 vcc, s4, v35
	v_add_f32_e32 v43, v53, v43
	v_add_f32_e32 v42, v42, v43
	v_add_f32_e32 v43, v45, v42
	v_mul_f32_e32 v53, v52, v43
	v_mul_f32_e32 v44, v51, v53
	v_fma_f32 v46, v53, v51, -v44
	v_fmac_f32_e32 v46, v53, v39
	v_sub_f32_e32 v39, v45, v43
	v_add_f32_e32 v39, v42, v39
	v_add_f32_e32 v42, v44, v46
	v_sub_f32_e32 v45, v43, v42
	v_pk_add_f32 v[48:49], v[42:43], v[44:45] neg_lo:[0,1] neg_hi:[0,1]
	v_mov_b32_e32 v47, v42
	v_pk_add_f32 v[42:43], v[48:49], v[46:47] neg_lo:[0,1] neg_hi:[0,1]
	s_nop 0
	v_add_f32_e32 v39, v39, v43
	v_add_f32_e32 v39, v42, v39
	v_add_f32_e32 v43, v54, v53
	v_add_f32_e32 v39, v45, v39
	v_sub_f32_e32 v42, v43, v54
	v_mul_f32_e32 v39, v52, v39
	v_sub_f32_e32 v42, v53, v42
	v_add_f32_e32 v44, v42, v39
	v_add_f32_e32 v46, v43, v44
	v_cvt_f32_i32_e32 v42, v50
	v_mul_f32_e32 v47, v46, v46
	v_sub_f32_e32 v43, v46, v43
	v_fmamk_f32 v39, v47, 0x3e9b6dac, v34
	v_sub_f32_e32 v43, v44, v43
	v_fmaak_f32 v39, v47, v39, 0x3f2aaada
	v_ldexp_f32 v48, v43, 1
	v_mul_f32_e32 v43, v46, v47
	v_ldexp_f32 v45, v46, 1
	v_pk_mul_f32 v[46:47], v[42:43], v[38:39]
	s_nop 0
	v_fma_f32 v44, v42, s11, -v46
	v_fmac_f32_e32 v44, 0xb102e308, v42
	v_pk_add_f32 v[42:43], v[46:47], v[44:45]
	s_nop 0
	v_sub_f32_e32 v39, v43, v45
	v_sub_f32_e32 v39, v47, v39
	v_add_f32_e32 v49, v48, v39
	v_mov_b32_e32 v48, v46
	v_pk_add_f32 v[46:47], v[42:43], v[46:47] neg_lo:[0,1] neg_hi:[0,1]
	v_pk_add_f32 v[50:51], v[42:43], v[48:49]
	v_mov_b32_e32 v45, v42
	v_mov_b32_e32 v47, v51
	v_pk_add_f32 v[52:53], v[44:45], v[46:47] neg_lo:[0,1] neg_hi:[0,1]
	v_pk_add_f32 v[44:45], v[44:45], v[46:47]
	v_mov_b32_e32 v48, v49
	v_pk_add_f32 v[46:47], v[44:45], v[42:43] op_sel:[1,0] op_sel_hi:[0,1] neg_lo:[0,1] neg_hi:[0,1]
	v_pk_add_f32 v[54:55], v[50:51], v[46:47] op_sel_hi:[1,0] neg_lo:[0,1] neg_hi:[0,1]
	v_mov_b32_e32 v50, v51
	v_mov_b32_e32 v51, v45
	v_pk_mov_b32 v[46:47], v[42:43], v[46:47] op_sel:[1,0]
	v_mov_b32_e32 v49, v42
	v_pk_add_f32 v[46:47], v[50:51], v[46:47] neg_lo:[0,1] neg_hi:[0,1]
	v_mov_b32_e32 v54, v52
	v_pk_add_f32 v[42:43], v[48:49], v[46:47] neg_lo:[0,1] neg_hi:[0,1]
	v_mov_b32_e32 v53, v45
	v_pk_add_f32 v[46:47], v[54:55], v[42:43]
	s_nop 0
	v_pk_add_f32 v[48:49], v[46:47], v[46:47] op_sel:[0,1] op_sel_hi:[1,0]
	s_nop 0
	v_pk_add_f32 v[44:45], v[44:45], v[48:49] op_sel:[1,0] op_sel_hi:[0,1]
	v_mov_b32_e32 v47, v44
	v_pk_add_f32 v[50:51], v[46:47], v[52:53] neg_lo:[0,1] neg_hi:[0,1]
	v_mov_b32_e32 v43, v48
	v_sub_f32_e32 v39, v46, v50
	v_pk_add_f32 v[42:43], v[42:43], v[50:51] neg_lo:[0,1] neg_hi:[0,1]
	v_sub_f32_e32 v39, v52, v39
	v_add_f32_e32 v39, v42, v39
	v_add_f32_e32 v39, v39, v43
	v_add_f32_e32 v39, v44, v39
	v_cndmask_b32_e32 v39, v107, v39, vcc
	v_cmp_lt_f32_e64 vcc, |v35|, s6
	s_nop 1
	v_cndmask_b32_e32 v35, v39, v35, vcc
	v_add_f32_e32 v35, 0x358637bd, v35
	v_med3_f32 v35, v35, s7, v103
	v_div_scale_f32 v39, s[14:15], v35, v35, s5
	v_rcp_f32_e32 v42, v39
	v_cmp_ngt_f32_e32 vcc, s2, v41
	s_nop 1
	v_cndmask_b32_e32 v43, 0, v57, vcc
	v_cmp_nlt_f32_e32 vcc, s3, v41
	v_fma_f32 v41, -v39, v42, 1.0
	v_fmac_f32_e32 v42, v41, v42
	v_cndmask_b32_e32 v102, v107, v43, vcc
	v_div_scale_f32 v41, vcc, s5, v35, s5
	v_mul_f32_e32 v43, v41, v42
	v_fma_f32 v44, -v39, v43, v41
	v_fmac_f32_e32 v43, v44, v42
	v_fma_f32 v39, -v39, v43, v41
	v_div_fmas_f32 v39, v39, v42, v43
	v_mul_f32_e32 v42, 0x3fb8aa3b, v36
	v_fma_f32 v43, v36, s1, -v42
	v_rndne_f32_e32 v44, v42
	v_fmac_f32_e32 v43, 0x32a5705f, v36
	v_sub_f32_e32 v42, v42, v44
	v_add_f32_e32 v42, v42, v43
	v_div_fixup_f32 v106, v39, v35, s5
	v_exp_f32_e32 v42, v42
	v_cvt_i32_f32_e32 v43, v44
	v_mul_f32_e32 v35, 0x3fb8aa3b, v106
	v_fma_f32 v39, v106, s1, -v35
	v_rndne_f32_e32 v41, v35
	v_fmac_f32_e32 v39, 0x32a5705f, v106
	v_sub_f32_e32 v35, v35, v41
	v_add_f32_e32 v35, v35, v39
	v_ldexp_f32 v39, v42, v43
	v_cmp_ngt_f32_e32 vcc, s2, v36
	v_exp_f32_e32 v35, v35
	v_cvt_i32_f32_e32 v41, v41
	v_cndmask_b32_e32 v39, 0, v39, vcc
	v_cmp_nlt_f32_e32 vcc, s3, v36
	v_ldexp_f32 v35, v35, v41
	s_nop 0
	v_cndmask_b32_e32 v36, v107, v39, vcc
	v_add_f32_e32 v39, 1.0, v36
	v_add_f32_e32 v42, -1.0, v39
	v_sub_f32_e32 v43, v42, v39
	v_add_f32_e32 v43, 1.0, v43
	v_sub_f32_e32 v42, v36, v42
	v_add_f32_e32 v44, v42, v43
	v_frexp_mant_f32_e32 v45, v39
	v_cvt_f64_f32_e32 v[42:43], v39
	v_frexp_exp_i32_f64_e32 v42, v[42:43]
	v_cmp_gt_f32_e32 vcc, s10, v45
	s_nop 1
	v_subbrev_co_u32_e32 v50, vcc, 0, v42, vcc
	v_sub_u32_e32 v42, 0, v50
	v_ldexp_f32 v39, v39, v42
	v_ldexp_f32 v42, v44, v42
	v_add_f32_e32 v44, -1.0, v39
	v_add_f32_e32 v43, 1.0, v44
	v_sub_f32_e32 v43, v39, v43
	v_add_f32_e32 v45, v42, v43
	v_add_f32_e32 v43, 1.0, v39
	v_add_f32_e32 v46, -1.0, v43
	v_sub_f32_e32 v39, v39, v46
	v_add_f32_e32 v39, v42, v39
	v_add_f32_e32 v51, v43, v39
	v_rcp_f32_e32 v52, v51
	v_sub_f32_e32 v42, v43, v51
	v_add_f32_e32 v43, v44, v45
	v_add_f32_e32 v39, v39, v42
	v_mul_f32_e32 v54, v43, v52
	v_sub_f32_e32 v42, v44, v43
	v_mul_f32_e32 v44, v51, v54
	v_fma_f32 v46, v54, v51, -v44
	v_fmac_f32_e32 v46, v54, v39
	v_add_f32_e32 v53, v45, v42
	v_add_f32_e32 v42, v44, v46
	v_sub_f32_e32 v45, v43, v42
	v_pk_add_f32 v[48:49], v[42:43], v[44:45] neg_lo:[0,1] neg_hi:[0,1]
	v_mov_b32_e32 v47, v42
	v_pk_add_f32 v[42:43], v[48:49], v[46:47] neg_lo:[0,1] neg_hi:[0,1]
	v_cmp_neq_f32_e32 vcc, s4, v36
	v_add_f32_e32 v43, v53, v43
	v_add_f32_e32 v42, v42, v43
	v_add_f32_e32 v43, v45, v42
	v_mul_f32_e32 v53, v52, v43
	v_mul_f32_e32 v44, v51, v53
	v_fma_f32 v46, v53, v51, -v44
	v_fmac_f32_e32 v46, v53, v39
	v_sub_f32_e32 v39, v45, v43
	v_add_f32_e32 v39, v42, v39
	v_add_f32_e32 v42, v44, v46
	v_sub_f32_e32 v45, v43, v42
	v_pk_add_f32 v[48:49], v[42:43], v[44:45] neg_lo:[0,1] neg_hi:[0,1]
	v_mov_b32_e32 v47, v42
	v_pk_add_f32 v[42:43], v[48:49], v[46:47] neg_lo:[0,1] neg_hi:[0,1]
	s_nop 0
	v_add_f32_e32 v39, v39, v43
	v_add_f32_e32 v39, v42, v39
	v_add_f32_e32 v43, v54, v53
	v_add_f32_e32 v39, v45, v39
	v_sub_f32_e32 v42, v43, v54
	v_mul_f32_e32 v39, v52, v39
	v_sub_f32_e32 v42, v53, v42
	v_add_f32_e32 v44, v42, v39
	v_add_f32_e32 v46, v43, v44
	v_cvt_f32_i32_e32 v42, v50
	v_mul_f32_e32 v47, v46, v46
	v_sub_f32_e32 v43, v46, v43
	v_fmamk_f32 v39, v47, 0x3e9b6dac, v34
	v_sub_f32_e32 v43, v44, v43
	v_fmaak_f32 v39, v47, v39, 0x3f2aaada
	v_ldexp_f32 v48, v43, 1
	v_mul_f32_e32 v43, v46, v47
	v_ldexp_f32 v45, v46, 1
	v_pk_mul_f32 v[46:47], v[42:43], v[38:39]
	s_nop 0
	v_fma_f32 v44, v42, s11, -v46
	v_fmac_f32_e32 v44, 0xb102e308, v42
	v_pk_add_f32 v[42:43], v[46:47], v[44:45]
	s_nop 0
	v_sub_f32_e32 v39, v43, v45
	v_sub_f32_e32 v39, v47, v39
	v_add_f32_e32 v49, v48, v39
	v_mov_b32_e32 v48, v46
	v_pk_add_f32 v[46:47], v[42:43], v[46:47] neg_lo:[0,1] neg_hi:[0,1]
	v_pk_add_f32 v[50:51], v[42:43], v[48:49]
	v_mov_b32_e32 v45, v42
	v_mov_b32_e32 v47, v51
	v_pk_add_f32 v[52:53], v[44:45], v[46:47] neg_lo:[0,1] neg_hi:[0,1]
	v_pk_add_f32 v[44:45], v[44:45], v[46:47]
	v_mov_b32_e32 v48, v49
	v_pk_add_f32 v[46:47], v[44:45], v[42:43] op_sel:[1,0] op_sel_hi:[0,1] neg_lo:[0,1] neg_hi:[0,1]
	v_pk_add_f32 v[54:55], v[50:51], v[46:47] op_sel_hi:[1,0] neg_lo:[0,1] neg_hi:[0,1]
	v_mov_b32_e32 v50, v51
	v_mov_b32_e32 v51, v45
	v_pk_mov_b32 v[46:47], v[42:43], v[46:47] op_sel:[1,0]
	v_mov_b32_e32 v49, v42
	v_pk_add_f32 v[46:47], v[50:51], v[46:47] neg_lo:[0,1] neg_hi:[0,1]
	v_mov_b32_e32 v54, v52
	v_pk_add_f32 v[42:43], v[48:49], v[46:47] neg_lo:[0,1] neg_hi:[0,1]
	v_mov_b32_e32 v53, v45
	v_pk_add_f32 v[46:47], v[54:55], v[42:43]
	s_nop 0
	v_pk_add_f32 v[48:49], v[46:47], v[46:47] op_sel:[0,1] op_sel_hi:[1,0]
	s_nop 0
	v_pk_add_f32 v[44:45], v[44:45], v[48:49] op_sel:[1,0] op_sel_hi:[0,1]
	v_mov_b32_e32 v47, v44
	v_pk_add_f32 v[50:51], v[46:47], v[52:53] neg_lo:[0,1] neg_hi:[0,1]
	v_mov_b32_e32 v43, v48
	v_sub_f32_e32 v39, v46, v50
	v_pk_add_f32 v[42:43], v[42:43], v[50:51] neg_lo:[0,1] neg_hi:[0,1]
	v_sub_f32_e32 v39, v52, v39
	v_add_f32_e32 v39, v42, v39
	v_add_f32_e32 v39, v39, v43
	v_add_f32_e32 v39, v44, v39
	v_cndmask_b32_e32 v39, v107, v39, vcc
	v_cmp_lt_f32_e64 vcc, |v36|, s6
	s_nop 1
	v_cndmask_b32_e32 v36, v39, v36, vcc
	v_add_f32_e32 v36, 0x358637bd, v36
	v_med3_f32 v36, v36, s7, v103
	v_div_scale_f32 v39, s[14:15], v36, v36, s5
	v_rcp_f32_e32 v42, v39
	v_cmp_ngt_f32_e32 vcc, s2, v106
	s_nop 1
	v_cndmask_b32_e32 v120, 0, v35, vcc
	v_fma_f32 v35, -v39, v42, 1.0
	v_fmac_f32_e32 v42, v35, v42
	v_div_scale_f32 v35, vcc, s5, v36, s5
	v_mul_f32_e32 v41, v35, v42
	v_fma_f32 v43, -v39, v41, v35
	v_fmac_f32_e32 v41, v43, v42
	v_fma_f32 v35, -v39, v41, v35
	v_div_fmas_f32 v35, v35, v42, v41
	v_mul_f32_e32 v41, 0x3fb8aa3b, v37
	v_fma_f32 v42, v37, s1, -v41
	v_rndne_f32_e32 v43, v41
	v_fmac_f32_e32 v42, 0x32a5705f, v37
	v_sub_f32_e32 v41, v41, v43
	v_div_fixup_f32 v121, v35, v36, s5
	v_add_f32_e32 v41, v41, v42
	v_mul_f32_e32 v35, 0x3fb8aa3b, v121
	v_exp_f32_e32 v41, v41
	v_cvt_i32_f32_e32 v42, v43
	v_fma_f32 v36, v121, s1, -v35
	v_rndne_f32_e32 v39, v35
	v_fmac_f32_e32 v36, 0x32a5705f, v121
	v_sub_f32_e32 v35, v35, v39
	v_add_f32_e32 v35, v35, v36
	v_exp_f32_e32 v122, v35
	v_ldexp_f32 v35, v41, v42
	v_cmp_ngt_f32_e32 vcc, s2, v37
	v_cvt_i32_f32_e32 v123, v39
	s_nop 0
	v_cndmask_b32_e32 v35, 0, v35, vcc
	v_cmp_nlt_f32_e32 vcc, s3, v37
	s_nop 1
	v_cndmask_b32_e32 v124, v107, v35, vcc
	v_add_f32_e32 v35, 1.0, v124
	v_add_f32_e32 v36, -1.0, v35
	v_sub_f32_e32 v37, v36, v35
	v_add_f32_e32 v37, 1.0, v37
	v_sub_f32_e32 v36, v124, v36
	v_add_f32_e32 v39, v36, v37
	v_frexp_mant_f32_e32 v41, v35
	v_cvt_f64_f32_e32 v[36:37], v35
	v_frexp_exp_i32_f64_e32 v36, v[36:37]
	v_cmp_gt_f32_e32 vcc, s10, v41
	s_nop 1
	v_subbrev_co_u32_e32 v41, vcc, 0, v36, vcc
	v_sub_u32_e32 v36, 0, v41
	v_ldexp_f32 v35, v35, v36
	v_ldexp_f32 v36, v39, v36
	v_add_f32_e32 v39, -1.0, v35
	v_add_f32_e32 v37, 1.0, v39
	v_sub_f32_e32 v37, v35, v37
	v_add_f32_e32 v42, v36, v37
	v_add_f32_e32 v37, 1.0, v35
	v_add_f32_e32 v43, -1.0, v37
	v_sub_f32_e32 v35, v35, v43
	v_add_f32_e32 v35, v36, v35
	v_add_f32_e32 v48, v37, v35
	v_rcp_f32_e32 v49, v48
	v_sub_f32_e32 v36, v37, v48
	v_add_f32_e32 v37, v39, v42
	v_add_f32_e32 v35, v35, v36
	v_sub_f32_e32 v36, v39, v37
	v_mul_f32_e32 v50, v37, v49
	v_add_f32_e32 v39, v42, v36
	v_mul_f32_e32 v42, v48, v50
	v_fma_f32 v44, v50, v48, -v42
	v_fmac_f32_e32 v44, v50, v35
	v_add_f32_e32 v36, v42, v44
	v_sub_f32_e32 v43, v37, v36
	v_pk_add_f32 v[46:47], v[36:37], v[42:43] neg_lo:[0,1] neg_hi:[0,1]
	v_mov_b32_e32 v45, v36
	v_pk_add_f32 v[36:37], v[46:47], v[44:45] neg_lo:[0,1] neg_hi:[0,1]
	v_cmp_neq_f32_e32 vcc, s4, v124
	v_add_f32_e32 v37, v39, v37
	v_add_f32_e32 v36, v36, v37
	v_add_f32_e32 v37, v43, v36
	v_mul_f32_e32 v39, v49, v37
	v_mul_f32_e32 v42, v48, v39
	v_fma_f32 v44, v39, v48, -v42
	v_fmac_f32_e32 v44, v39, v35
	v_sub_f32_e32 v35, v43, v37
	v_add_f32_e32 v35, v36, v35
	v_add_f32_e32 v36, v42, v44
	v_sub_f32_e32 v43, v37, v36
	v_pk_add_f32 v[46:47], v[36:37], v[42:43] neg_lo:[0,1] neg_hi:[0,1]
	v_mov_b32_e32 v45, v36
	v_pk_add_f32 v[36:37], v[46:47], v[44:45] neg_lo:[0,1] neg_hi:[0,1]
	s_nop 0
	v_add_f32_e32 v35, v35, v37
	v_add_f32_e32 v35, v36, v35
	v_add_f32_e32 v36, v50, v39
	v_add_f32_e32 v35, v43, v35
	v_sub_f32_e32 v37, v36, v50
	v_mul_f32_e32 v35, v49, v35
	v_sub_f32_e32 v37, v39, v37
	v_add_f32_e32 v35, v37, v35
	v_add_f32_e32 v39, v36, v35
	v_mul_f32_e32 v42, v39, v39
	v_fmac_f32_e32 v34, 0x3e9b6dac, v42
	v_fmac_f32_e32 v56, v42, v34
	v_cvt_f32_i32_e32 v34, v41
	v_sub_f32_e32 v36, v39, v36
	v_sub_f32_e32 v35, v35, v36
	v_ldexp_f32 v37, v39, 1
	v_ldexp_f32 v41, v35, 1
	v_mul_f32_e32 v35, v39, v42
	v_mov_b32_e32 v39, v56
	v_pk_mul_f32 v[38:39], v[34:35], v[38:39]
	s_nop 0
	v_fma_f32 v36, v34, s11, -v38
	v_fmac_f32_e32 v36, 0xb102e308, v34
	v_pk_add_f32 v[104:105], v[38:39], v[36:37]
	s_nop 0
	v_sub_f32_e32 v34, v105, v37
	v_sub_f32_e32 v34, v39, v34
	v_add_f32_e32 v35, v41, v34
	v_mov_b32_e32 v34, v38
	v_pk_add_f32 v[38:39], v[104:105], v[38:39] neg_lo:[0,1] neg_hi:[0,1]
	v_pk_add_f32 v[42:43], v[104:105], v[34:35]
	v_mov_b32_e32 v37, v104
	v_mov_b32_e32 v39, v43
	v_pk_add_f32 v[110:111], v[36:37], v[38:39]
	v_pk_add_f32 v[108:109], v[36:37], v[38:39] neg_lo:[0,1] neg_hi:[0,1]
	v_pk_add_f32 v[36:37], v[110:111], v[104:105] op_sel:[1,0] op_sel_hi:[0,1] neg_lo:[0,1] neg_hi:[0,1]
	v_pk_add_f32 v[112:113], v[42:43], v[36:37] op_sel_hi:[1,0] neg_lo:[0,1] neg_hi:[0,1]
	v_mov_b32_e32 v38, v43
	v_mov_b32_e32 v39, v111
	v_pk_mov_b32 v[36:37], v[104:105], v[36:37] op_sel:[1,0]
	v_mov_b32_e32 v116, v35
	v_lshl_add_u64 v[34:35], s[52:53], 0, v[62:63]
	v_pk_add_f32 v[114:115], v[38:39], v[36:37] neg_lo:[0,1] neg_hi:[0,1]
	v_lshl_add_u64 v[34:35], v[34:35], 0, v[118:119]
	v_lshlrev_b32_e32 v36, 4, v1
	v_mov_b32_e32 v37, v63
	v_lshl_add_u64 v[34:35], v[34:35], 0, v[36:37]
	s_barrier
	global_load_dwordx4 v[98:101], v[34:35], off
	global_load_dwordx4 v[70:73], v[34:35], off offset:256
	global_load_dwordx4 v[78:81], v[34:35], off offset:512
	global_load_dwordx4 v[86:89], v[34:35], off offset:768
	global_load_dwordx4 v[94:97], v[34:35], off offset:1024
	global_load_dwordx4 v[90:93], v[34:35], off offset:1280
	global_load_dwordx4 v[82:85], v[34:35], off offset:1536
	global_load_dwordx4 v[74:77], v[34:35], off offset:1792
	global_load_dwordx4 v[66:69], v[34:35], off offset:2048
	global_load_dwordx4 v[58:61], v[34:35], off offset:2304
	global_load_dwordx4 v[54:57], v[34:35], off offset:2560
	global_load_dwordx4 v[50:53], v[34:35], off offset:2816
	global_load_dwordx4 v[46:49], v[34:35], off offset:3072
	global_load_dwordx4 v[42:45], v[34:35], off offset:3328
	global_load_dwordx4 v[38:41], v[34:35], off offset:3584
	s_nop 0
	global_load_dwordx4 v[34:37], v[34:35], off offset:3840
	v_mov_b32_e32 v117, v104
	v_pk_add_f32 v[104:105], v[116:117], v[114:115] neg_lo:[0,1] neg_hi:[0,1]
	v_mov_b32_e32 v112, v108
	v_pk_add_f32 v[112:113], v[112:113], v[104:105]
	v_mov_b32_e32 v109, v111
	v_pk_add_f32 v[114:115], v[112:113], v[112:113] op_sel:[0,1] op_sel_hi:[1,0]
	v_lshlrev_b32_e32 v1, 5, v1
	v_pk_add_f32 v[110:111], v[110:111], v[114:115] op_sel:[1,0] op_sel_hi:[0,1]
	v_mov_b32_e32 v113, v110
	v_pk_add_f32 v[116:117], v[112:113], v[108:109] neg_lo:[0,1] neg_hi:[0,1]
	v_mov_b32_e32 v105, v114
	v_sub_f32_e32 v109, v112, v116
	v_pk_add_f32 v[104:105], v[104:105], v[116:117] neg_lo:[0,1] neg_hi:[0,1]
	v_sub_f32_e32 v108, v108, v109
	v_add_f32_e32 v104, v104, v108
	v_add_f32_e32 v104, v104, v105
	v_add_f32_e32 v104, v110, v104
	v_cndmask_b32_e32 v104, v107, v104, vcc
	v_cmp_lt_f32_e64 vcc, |v124|, s6
	v_lshlrev_b32_e32 v114, 3, v64
	v_or3_b32 v62, v118, v0, v62
	v_cndmask_b32_e32 v104, v104, v124, vcc
	v_add_f32_e32 v104, 0x358637bd, v104
	v_med3_f32 v108, v104, s7, v103
	v_div_scale_f32 v109, s[6:7], v108, v108, s5
	v_rcp_f32_e32 v110, v109
	v_cmp_nlt_f32_e32 vcc, s3, v106
	v_ldexp_f32 v106, v122, v123
	v_or3_b32 v122, v65, v1, v114
	v_fma_f32 v111, -v109, v110, 1.0
	v_cndmask_b32_e32 v103, v107, v120, vcc
	v_fmac_f32_e32 v110, v111, v110
	v_div_scale_f32 v111, vcc, s5, v108, s5
	v_mul_f32_e32 v112, v111, v110
	v_fma_f32 v113, -v109, v112, v111
	v_fmac_f32_e32 v112, v113, v110
	v_fma_f32 v109, -v109, v112, v111
	v_div_fmas_f32 v109, v109, v110, v112
	v_div_fixup_f32 v108, v109, v108, s5
	v_mul_f32_e32 v109, 0x3fb8aa3b, v108
	v_fma_f32 v110, v108, s1, -v109
	v_rndne_f32_e32 v111, v109
	v_fmac_f32_e32 v110, 0x32a5705f, v108
	v_sub_f32_e32 v109, v109, v111
	v_add_f32_e32 v109, v109, v110
	v_exp_f32_e32 v109, v109
	v_cvt_i32_f32_e32 v110, v111
	v_cmp_ngt_f32_e32 vcc, s2, v121
	v_pk_add_f32 v[104:105], v[102:103], 1.0 op_sel_hi:[1,0] neg_lo:[1,0] neg_hi:[1,0]
	v_lshl_add_u64 v[0:1], s[52:53], 0, v[62:63]
	v_cndmask_b32_e32 v106, 0, v106, vcc
	v_cmp_nlt_f32_e32 vcc, s3, v121
	v_ldexp_f32 v109, v109, v110
	s_mov_b64 s[6:7], 0x1800
	v_cndmask_b32_e32 v106, v107, v106, vcc
	v_cmp_ngt_f32_e32 vcc, s2, v108
	v_pk_mul_f32 v[110:111], v[104:105], -2.0 op_sel_hi:[1,0]
	v_cmp_eq_u32_e64 s[0:1], 0, v64
	v_cndmask_b32_e32 v109, 0, v109, vcc
	v_cmp_nlt_f32_e32 vcc, s3, v108
	v_cmp_gt_u32_e64 s[2:3], 2, v64
	v_cmp_eq_u32_e64 s[4:5], 3, v64
	v_cndmask_b32_e32 v107, v107, v109, vcc
	v_pk_add_f32 v[108:109], v[106:107], 1.0 op_sel_hi:[1,0] neg_lo:[1,0] neg_hi:[1,0]
	v_lshl_add_u64 v[0:1], v[0:1], 0, s[6:7]
	v_pk_mul_f32 v[112:113], v[108:109], -2.0 op_sel_hi:[1,0]
	s_mov_b64 s[6:7], 0x1000
	v_mov_b32_e32 v165, v3
	v_mov_b32_e32 v166, v4
	v_mov_b32_e32 v167, v5
	v_mov_b32_e32 v168, v6
	v_mov_b32_e32 v169, v7
	v_mov_b32_e32 v170, v8
	v_mov_b32_e32 v3, v166
	v_mov_b32_e32 v4, v168
	v_mov_b32_e32 v5, v170
	v_mov_b32_e32 v6, v165
	v_mov_b32_e32 v7, v167
	v_mov_b32_e32 v8, v169
	v_mov_b32_e32 v165, v11
	v_mov_b32_e32 v166, v12
	v_mov_b32_e32 v167, v13
	v_mov_b32_e32 v168, v14
	v_mov_b32_e32 v169, v15
	v_mov_b32_e32 v170, v16
	v_mov_b32_e32 v11, v166
	v_mov_b32_e32 v12, v168
	v_mov_b32_e32 v13, v170
	v_mov_b32_e32 v14, v165
	v_mov_b32_e32 v15, v167
	v_mov_b32_e32 v16, v169
	v_mov_b32_e32 v165, v19
	v_mov_b32_e32 v166, v20
	v_mov_b32_e32 v167, v21
	v_mov_b32_e32 v168, v22
	v_mov_b32_e32 v169, v23
	v_mov_b32_e32 v170, v24
	v_mov_b32_e32 v19, v166
	v_mov_b32_e32 v20, v168
	v_mov_b32_e32 v21, v170
	v_mov_b32_e32 v22, v165
	v_mov_b32_e32 v23, v167
	v_mov_b32_e32 v24, v169
	v_mov_b32_e32 v165, v27
	v_mov_b32_e32 v166, v28
	v_mov_b32_e32 v167, v29
	v_mov_b32_e32 v168, v30
	v_mov_b32_e32 v169, v31
	v_mov_b32_e32 v170, v32
	v_mov_b32_e32 v27, v166
	v_mov_b32_e32 v28, v168
	v_mov_b32_e32 v29, v170
	v_mov_b32_e32 v30, v165
	v_mov_b32_e32 v31, v167
	v_mov_b32_e32 v32, v169
	v_mov_b32_e32 v124, 0
	v_mov_b32_e32 v125, 0
	v_mov_b32_e32 v126, 0
	v_mov_b32_e32 v127, 0
	v_mov_b32_e32 v128, 0
	v_mov_b32_e32 v129, 0
	v_mov_b32_e32 v130, 0
	v_mov_b32_e32 v131, 0
	v_mov_b32_e32 v148, 0
	v_mov_b32_e32 v149, 0
	v_mov_b32_e32 v150, 0
	v_mov_b32_e32 v151, 0
	v_mov_b32_e32 v152, v104
	v_mov_b32_e32 v153, v105
	v_mov_b32_e32 v154, v108
	v_mov_b32_e32 v155, v109
	s_branch .LBB3_169
